# 5-slot LDS pack ring (14 KiB pitch, slot = chunk mod 5) on the chunk-136 split with 2 conversion blocks per wave in the P1 tail
# baseline (speedup 1.0000x reference)
; #define LAS __attribute__((address_space(3)))
; __global__ void __launch_bounds__(NTHR, 2) mk_fwd(Args args) {
;     ...
;         const int xcd_i = bx % 8, slot_i = bx / 8;
;         constexpr int NSCAN_X = 8;
;         if (slot_i < NSCAN_X) {
;             constexpr int CH = 16, NCHUNK = SEQ / CH, NSLOT = 8, LAG = 3;
;             LAS unsigned* ring_ready = (LAS unsigned*)(lds + LDSCTL_OFF + 896); LAS unsigned* ring_done = ring_ready + 4;
;             constexpr int PK_PA = 0, PK_PR = 2048, PK_QQ = 4096, PK_TT = 5120, PK_GG = 6144, PK_BK = 7168, PK_VT = 11264, PK_WC = 13312, PK_BON = 13568, PK_BYTES = 16384;
;             const int hd = xcd_i * NSCAN_X + slot_i, b = hd >> 4, h = hd & 15;
;             const size_t mbase = (size_t)b * SEQ;
;             static_assert((size_t)64 * NCHUNK * PK_BYTES <= 4 * SZ_F1K, "packs fit the four unused f32 [M][1024] buffers at WS_R");
;             unsigned char* PACK = ws + WS_R + (size_t)hd * NCHUNK * PK_BYTES;
;             const int tr = lane & 15, q = lane >> 4;
;             if (wave < 4) {
;     ...
;             } else {
;                 const int lw = wave - 4;
.LBB0_586:
	s_andn2_b64 vcc, exec, s[2:3]
	s_cbranch_vccnz .LBB0_670
	v_readlane_b32 s2, v252, 38
	s_lshl_b32 s2, s2, 3
	v_readlane_b32 s3, v252, 39
	s_add_i32 s6, s2, s3
	v_readlane_b32 s10, v252, 42
	s_cmpk_gt_u32 s10, 0xff
	s_mov_b64 s[2:3], -1
	s_cbranch_scc0 .LBB0_611
	v_writelane_b32 v252, s0, 54
	v_writelane_b32 v252, s1, 55
	v_writelane_b32 v252, s28, 56
	v_writelane_b32 v252, s29, 57
	v_writelane_b32 v252, s30, 58
	v_writelane_b32 v252, s72, 59
	v_writelane_b32 v252, s86, 60
	v_writelane_b32 v252, s90, 61
	v_writelane_b32 v252, s91, 62
	v_readlane_b32 s4, v252, 43
	s_nop 3
	s_sub_i32 s4, s4, 4
	s_lshr_b32 s5, s6, 4
	s_and_b32 s7, s6, 15
	s_lshl_b32 s5, s5, 12
	s_or_b32 s5, s5, s7
	s_lshl_b32 s7, s4, 4
	s_or_b32 s30, s5, s7
	s_movk_i32 s28, 64
	s_add_u32 s10, s26, 0x6008000
	s_addc_u32 s11, s27, 0
	s_and_b32 s101, s30, 0xfffff000
	s_add_i32 s101, s101, 2176
	s_mul_i32 s100, s4, 14336
	s_lshl_b32 s98, s4, 2
	s_add_i32 s98, s98, 0x27380
	v_mov_b32_e32 v1, s98
	v_mov_b32_e32 v2, s4
	ds_write_b32 v1, v2
	s_waitcnt vmcnt(0) lgkmcnt(0)
	s_branch .Lprod_code

; #define LAS __attribute__((address_space(3)))
; __global__ void __launch_bounds__(NTHR, 2) mk_fwd(Args args) {
;     ...
;                 for (int c = 0; c < NCHUNK + LAG; ++c) {
;                     if (c < NCHUNK) {
;                         if (c >= NSLOT) { const unsigned want = (unsigned)(c - NSLOT + 1); unsigned sp_ = 0;
;                             for (;;) { const v4u dd_ = *(volatile LAS v4u*)ring_done; if (min(min(dd_.x, dd_.y), min(dd_.z, dd_.w)) >= want) break; __builtin_amdgcn_s_sleep(0); if (++sp_ > (1u << 26)) break; } }
;                         asm volatile("" ::: "memory");
.Lld_loop:
	s_sub_i32 s8, s39, 4
	v_mov_b32_e32 v1, 0x27390
	s_mov_b32 s5, 0

; #define LAS __attribute__((address_space(3)))
; __global__ void __launch_bounds__(NTHR, 2) mk_fwd(Args args) {
;     ...
;                         const unsigned char* src = PACK + (size_t)c * PK_BYTES + lw * 1024 + lane * 16;
;                         LAS unsigned char* dst = lds + (c & (NSLOT - 1)) * PK_BYTES + lw * 1024;
; #pragma unroll
;                         for (int p = 0; p < 3; ++p) __builtin_amdgcn_global_load_lds((const unsigned*)(src + p * 4096), (LAS unsigned*)(dst + p * 4096), 16, 0, 0);
;                         if (lw < 2) __builtin_amdgcn_global_load_lds((const unsigned*)(src + 3 * 4096), (LAS unsigned*)(dst + 3 * 4096), 16, 0, 0);
;                     }
;                     if (c >= LAG) {
;                         if (c < NCHUNK) { if (lw < 2) asm volatile("s_waitcnt vmcnt(12)" ::: "memory"); else asm volatile("s_waitcnt vmcnt(9)" ::: "memory"); } else asm volatile("s_waitcnt vmcnt(0)" ::: "memory");
;                         if (lane == 0) __hip_atomic_fetch_add(ring_ready + lw, 1u, __ATOMIC_RELAXED, __HIP_MEMORY_SCOPE_WORKGROUP);
;                     }
.Lld_sok:
	s_lshl_b32 s8, s39, 14
	v_lshl_add_u64 v[4:5], v[2:3], 0, s[8:9]
	s_mul_i32 s8, s39, 205
	s_lshr_b32 s8, s8, 10
	s_mul_i32 s8, s8, 5
	s_sub_i32 s8, s39, s8
	s_mul_i32 s8, s8, 14336
	s_add_i32 s8, s8, s7
	s_mov_b32 m0, s8
	v_lshl_add_u64 v[6:7], v[4:5], 0, s[12:13]
	global_load_lds_dwordx4 v[4:5], off
	s_add_i32 m0, s8, 0x1000
	s_nop 0
	global_load_lds_dwordx4 v[6:7], off
	v_lshl_add_u64 v[6:7], v[4:5], 0, s[14:15]
	s_add_i32 m0, s8, 0x2000
	s_nop 0
	global_load_lds_dwordx4 v[6:7], off
	s_cmpk_gt_u32 s7, 0x400
	s_cbranch_scc1 .Lld_three
	v_lshl_add_u64 v[6:7], v[4:5], 0, s[16:17]
	s_add_i32 m0, s8, 0x3000
	s_nop 0
	global_load_lds_dwordx4 v[6:7], off
	s_cmpk_eq_i32 s39, 136
	s_cbranch_scc1 .Lld_next
	s_waitcnt vmcnt(4)
	s_branch .Lld_pub

.LBB0_623:
	s_add_i32 s8, s5, -1
	s_mul_i32 s12, s8, 205
	s_lshr_b32 s12, s12, 10
	s_mul_i32 s12, s12, 5
	s_sub_i32 s12, s8, s12
	s_mul_i32 s12, s12, 14336
	s_add_i32 s12, s12, 0
	v_lshlrev_b32_e32 v30, 1, v176
	v_add3_u32 v87, s12, v181, v30
	ds_read_u16 v30, v87 offset:11264
	ds_read_u16 v31, v87 offset:11296
	ds_read_u16 v82, v87 offset:11328
	s_lshl_b32 s13, s8, 12
	s_and_b32 s13, s13, 0x3000
	v_add_u32_e32 v78, s13, v190
	v_add_u32_e32 v88, s12, v180
	s_waitcnt lgkmcnt(0)
	v_lshlrev_b32_e32 v86, 16, v82
	s_add_i32 s13, s35, s12
	v_add_u32_e32 v82, s12, v1
	ds_read_b128 v[78:81], v78
	v_add3_u32 v90, s13, v178, v179
	ds_read_b128 v[82:85], v82 offset:13312
	ds_read_u16 v87, v87 offset:11360
	ds_read_b64 v[88:89], v88 offset:2048
	ds_read_u16 v92, v90 offset:7176
	ds_read_u16 v93, v90 offset:7240
	ds_read_u16 v94, v90 offset:7304
	ds_read_u16 v95, v90 offset:7368
	s_waitcnt lgkmcnt(6)
	v_rcp_f32_e32 v82, v82
	v_rcp_f32_e32 v83, v83
	s_waitcnt lgkmcnt(4)
	v_lshlrev_b32_e32 v90, 16, v88
	v_and_b32_e32 v91, 0xffff0000, v88
	s_waitcnt lgkmcnt(2)
	v_lshlrev_b32_e32 v93, 16, v93
	v_lshlrev_b32_e32 v92, 16, v92
	v_pk_mul_f32 v[90:91], v[90:91], v[92:93]
	v_rcp_f32_e32 v84, v84
	s_waitcnt vmcnt(1)
	v_pk_mul_f32 v[90:91], v[10:11], v[90:91]
	v_rcp_f32_e32 v85, v85
	v_pk_mul_f32 v[82:83], v[82:83], v[90:91]
	v_lshlrev_b32_e32 v88, 16, v89
	v_and_b32_e32 v89, 0xffff0000, v89
	s_waitcnt lgkmcnt(0)
	v_lshlrev_b32_e32 v91, 16, v95
	v_lshlrev_b32_e32 v90, 16, v94
	v_pk_mul_f32 v[88:89], v[88:89], v[90:91]
	v_add_f32_e32 v82, v82, v83
	v_pk_mul_f32 v[88:89], v[12:13], v[88:89]
	v_lshlrev_b32_e32 v30, 16, v30
	v_pk_mul_f32 v[84:85], v[84:85], v[88:89]
	v_lshlrev_b32_e32 v31, 16, v31
	v_add_f32_e32 v82, v82, v84
	v_add_f32_e32 v82, v82, v85
	v_lshlrev_b32_e32 v87, 16, v87
	s_lshl_b64 s[12:13], s[8:9], 16
	v_add_f32_dpp v88, v82, v82 quad_perm:[1,0,3,2] row_mask:0xf bank_mask:0xf bound_ctrl:1
	v_add_f32_e32 v82, v78, v79
	v_add_f32_e32 v82, v80, v82
	v_add_f32_e32 v82, v81, v82
	s_nop 1
	v_add_f32_dpp v82, v82, v82 quad_perm:[1,0,3,2] row_mask:0xf bank_mask:0xf bound_ctrl:1
	s_nop 1
	v_add_f32_dpp v82, v82, v82 quad_perm:[2,3,0,1] row_mask:0xf bank_mask:0xf bound_ctrl:1
	s_nop 1
	v_add_f32_dpp v82, v82, v82 row_half_mirror row_mask:0xf bank_mask:0xf bound_ctrl:1
	s_nop 1
	v_add_f32_dpp v82, v82, v82 row_mirror row_mask:0xf bank_mask:0xf bound_ctrl:1
	v_fmamk_f32 v79, v82, 0xbc800000, v79
	v_fmamk_f32 v78, v82, 0xbc800000, v78
	v_fmamk_f32 v81, v82, 0xbc800000, v81
	v_fmac_f32_e32 v80, 0xbc800000, v82
	v_pk_mul_f32 v[84:85], v[78:79], v[78:79]
	v_pk_mul_f32 v[82:83], v[80:81], v[80:81]
	v_add_f32_e32 v84, v84, v85
	v_add_f32_e32 v82, v82, v84
	v_add_f32_e32 v82, v83, v82
	v_add_f32_dpp v83, v88, v88 quad_perm:[2,3,0,1] row_mask:0xf bank_mask:0xf bound_ctrl:1
	s_nop 0
	v_add_f32_dpp v82, v82, v82 quad_perm:[1,0,3,2] row_mask:0xf bank_mask:0xf bound_ctrl:1
	v_add_f32_dpp v83, v83, v83 row_half_mirror row_mask:0xf bank_mask:0xf bound_ctrl:1
	s_nop 0
	v_add_f32_dpp v82, v82, v82 quad_perm:[2,3,0,1] row_mask:0xf bank_mask:0xf bound_ctrl:1
	v_add_f32_dpp v84, v83, v83 row_mirror row_mask:0xf bank_mask:0xf bound_ctrl:1
	s_nop 0
	v_add_f32_dpp v82, v82, v82 row_half_mirror row_mask:0xf bank_mask:0xf bound_ctrl:1
	s_nop 1
	v_add_f32_dpp v82, v82, v82 row_mirror row_mask:0xf bank_mask:0xf bound_ctrl:1
	v_fmamk_f32 v82, v82, 0x3c800000, v193
	v_rsq_f32_e32 v82, v82
	s_nop 0
	v_pk_mul_f32 v[78:79], v[78:79], v[82:83] op_sel_hi:[1,0]
	v_pk_mul_f32 v[80:81], v[80:81], v[82:83] op_sel_hi:[1,0]
	v_pk_fma_f32 v[78:79], v[2:3], v[78:79], v[6:7]
	v_pk_fma_f32 v[80:81], v[4:5], v[80:81], v[8:9]
	v_pk_fma_f32 v[30:31], v[84:85], v[30:31], v[78:79] op_sel_hi:[0,1,1]
	v_pk_fma_f32 v[78:79], v[84:85], v[86:87], v[80:81] op_sel_hi:[0,1,1]
	v_lshlrev_b32_e32 v80, 16, v172
	v_and_b32_e32 v81, 0xffff0000, v172
	v_lshlrev_b32_e32 v82, 16, v173
	v_and_b32_e32 v83, 0xffff0000, v173
	v_pk_mul_f32 v[78:79], v[78:79], v[82:83]
	v_pk_mul_f32 v[30:31], v[30:31], v[80:81]
	s_nop 0
	v_cvt_pk_bf16_f32 v30, v30, v31
	v_cvt_pk_bf16_f32 v31, v78, v79
	v_lshl_add_u64 v[78:79], v[170:171], 0, s[12:13]
	global_store_dwordx2 v[78:79], v[30:31], off
	s_waitcnt lgkmcnt(0)
	s_and_saveexec_b64 s[12:13], s[2:3]
	v_mov_b32_e32 v30, s34
	v_mov_b32_e32 v31, 1
	ds_add_u32 v30, v31
	v_mov_b32_e32 v30, s31
	ds_add_u32 v30, v31

.LBB0_633:
	s_or_b32 s43, s5, 1
	v_lshl_or_b32 v30, s43, 4, v176
	v_or_b32_e32 v78, s6, v30
	v_mov_b64_e32 v[30:31], s[66:67]
	v_mad_u64_u32 v[30:31], s[12:13], v78, s36, v[30:31]
	v_mad_i32_i24 v31, s7, v177, v31
	v_lshl_add_u64 v[30:31], v[30:31], 0, s[10:11]
	v_lshl_add_u64 v[30:31], v[30:31], 0, v[162:163]
	v_add_co_u32_e32 v30, vcc, s37, v30
	v_cvt_pk_bf16_f32 v198, v106, v107
	s_nop 0
	v_addc_co_u32_e32 v31, vcc, 0, v31, vcc
	global_load_dwordx2 v[172:173], v[30:31], off
	v_cvt_pk_bf16_f32 v199, v108, v109
	v_cvt_pk_bf16_f32 v200, v110, v111
	v_cvt_pk_bf16_f32 v201, v112, v113
	s_mul_i32 s8, s43, 205
	s_lshr_b32 s8, s8, 10
	s_mul_i32 s8, s8, 5
	s_sub_i32 s8, s43, s8
	s_mul_i32 s8, s8, 14336
	v_mfma_f32_16x16x32_bf16 v[70:73], v[70:73], v[198:201], 0
	s_add_i32 s12, s8, 0
	v_cvt_pk_bf16_f32 v158, v114, v115
	v_cvt_pk_bf16_f32 v159, v116, v117
	v_cvt_pk_bf16_f32 v160, v118, v119
	v_cvt_pk_bf16_f32 v161, v120, v121
	v_add_u32_e32 v30, s12, v184
	ds_read_b128 v[154:157], v30
	ds_read_b128 v[146:149], v30 offset:64
	ds_read_b128 v[138:141], v30 offset:2048
	ds_read_b128 v[98:101], v30 offset:2112
	v_mfma_f32_16x16x32_bf16 v[62:65], v[62:65], v[158:161], v[70:73]
	v_add_u32_e32 v30, s12, v185
	ds_read_b128 v[150:153], v30 offset:4096
	ds_read_b128 v[142:145], v30 offset:5120
	ds_read_b128 v[102:105], v30 offset:6144
	ds_read_b128 v[94:97], v30 offset:7168
	v_add_u32_e32 v30, s12, v187
	v_add3_u32 v31, s12, v188, v183
	ds_read_b128 v[90:93], v30 offset:8192
	ds_read_b128 v[86:89], v30 offset:9216
	ds_read_b128 v[78:81], v30 offset:10240
	ds_read_b64 v[84:85], v31 offset:11264
	v_mov_b32_e32 v30, v32
	v_mov_b32_e32 v31, v33
	v_add_u32_e32 v70, s12, v186
	ds_read_b128 v[134:137], v70 offset:13312
	ds_read_b128 v[130:133], v70 offset:13376
	ds_read_b128 v[126:129], v70 offset:13440
	ds_read_b128 v[122:125], v70 offset:13504
	v_mfma_f32_16x16x32_bf16 v[62:65], v[74:77], v[30:33], v[62:65]
	s_mov_b32 s8, 0
	v_mfma_f32_16x16x32_bf16 v[58:61], v[58:61], v[198:201], 0
	s_nop 5
	v_cvt_pk_bf16_f32 v62, v62, v63
	v_cvt_pk_bf16_f32 v63, v64, v65
	v_mov_b32_e32 v64, v163
	v_mov_b32_e32 v65, v163
	s_nop 1
	v_mfma_f32_16x16x32_bf16 v[62:65], v[66:69], v[62:65], 0
	s_cmp_lt_u32 s5, s99
	s_cbranch_scc1 .Lscan_y1_skip
	s_branch .LBB0_635

.LBB0_644:
	s_mul_i32 s12, s5, 205
	s_lshr_b32 s12, s12, 10
	s_mul_i32 s12, s12, 5
	s_sub_i32 s12, s5, s12
	s_mul_i32 s12, s12, 14336
	s_add_i32 s12, s12, 0
	v_lshlrev_b32_e32 v31, 1, v176
	v_add3_u32 v25, s12, v181, v31
	ds_read_u16 v18, v25 offset:11264
	ds_read_u16 v19, v25 offset:11296
	ds_read_u16 v20, v25 offset:11328
	v_lshlrev_b32_e32 v30, 2, v189
	v_add3_u32 v14, s8, v30, v182
	s_waitcnt lgkmcnt(2)
	v_lshlrev_b32_e32 v22, 16, v18
	v_add_u32_e32 v26, s12, v180
	s_add_i32 s8, s35, s12
	v_add_u32_e32 v18, s12, v1
	ds_read_b128 v[14:17], v14
	s_waitcnt lgkmcnt(2)
	v_lshlrev_b32_e32 v23, 16, v19
	s_waitcnt lgkmcnt(1)
	v_lshlrev_b32_e32 v24, 16, v20
	v_add3_u32 v28, s8, v178, v179
	ds_read_b128 v[18:21], v18 offset:13312
	ds_read_u16 v25, v25 offset:11360
	ds_read_b64 v[26:27], v26 offset:2048
	ds_read_u16 v32, v28 offset:7176
	ds_read_u16 v33, v28 offset:7240
	ds_read_u16 v34, v28 offset:7304
	ds_read_u16 v35, v28 offset:7368
	s_waitcnt lgkmcnt(6)
	v_rcp_f32_e32 v18, v18
	v_rcp_f32_e32 v19, v19
	s_waitcnt lgkmcnt(4)
	v_lshlrev_b32_e32 v28, 16, v26
	v_and_b32_e32 v29, 0xffff0000, v26
	s_waitcnt lgkmcnt(2)
	v_lshlrev_b32_e32 v33, 16, v33
	v_lshlrev_b32_e32 v32, 16, v32
	v_pk_mul_f32 v[28:29], v[28:29], v[32:33]
	v_rcp_f32_e32 v20, v20
	s_waitcnt vmcnt(2)
	v_pk_mul_f32 v[28:29], v[10:11], v[28:29]
	v_rcp_f32_e32 v21, v21
	v_pk_mul_f32 v[18:19], v[18:19], v[28:29]
	v_lshlrev_b32_e32 v26, 16, v27
	v_and_b32_e32 v27, 0xffff0000, v27
	s_waitcnt lgkmcnt(0)
	v_lshlrev_b32_e32 v29, 16, v35
	v_lshlrev_b32_e32 v28, 16, v34
	v_pk_mul_f32 v[26:27], v[26:27], v[28:29]
	v_add_f32_e32 v18, v18, v19
	v_pk_mul_f32 v[26:27], v[12:13], v[26:27]
	v_lshlrev_b32_e32 v25, 16, v25
	v_pk_mul_f32 v[20:21], v[20:21], v[26:27]
	s_nop 0
	v_add_f32_e32 v18, v18, v20
	v_add_f32_e32 v18, v18, v21
	s_nop 1
	v_add_f32_dpp v26, v18, v18 quad_perm:[1,0,3,2] row_mask:0xf bank_mask:0xf bound_ctrl:1
	v_add_f32_e32 v18, v14, v15
	v_add_f32_e32 v18, v16, v18
	v_add_f32_e32 v18, v17, v18
	s_nop 1
	v_add_f32_dpp v18, v18, v18 quad_perm:[1,0,3,2] row_mask:0xf bank_mask:0xf bound_ctrl:1
	s_nop 1
	v_add_f32_dpp v18, v18, v18 quad_perm:[2,3,0,1] row_mask:0xf bank_mask:0xf bound_ctrl:1
	s_nop 1
	v_add_f32_dpp v18, v18, v18 row_half_mirror row_mask:0xf bank_mask:0xf bound_ctrl:1
	s_nop 1
	v_add_f32_dpp v18, v18, v18 row_mirror row_mask:0xf bank_mask:0xf bound_ctrl:1
	v_fmamk_f32 v15, v18, 0xbc800000, v15
	v_fmamk_f32 v14, v18, 0xbc800000, v14
	v_fmamk_f32 v17, v18, 0xbc800000, v17
	v_fmac_f32_e32 v16, 0xbc800000, v18
	v_pk_mul_f32 v[20:21], v[14:15], v[14:15]
	v_pk_mul_f32 v[18:19], v[16:17], v[16:17]
	v_add_f32_e32 v20, v20, v21
	v_add_f32_e32 v18, v18, v20
	v_add_f32_e32 v18, v19, v18
	v_add_f32_dpp v19, v26, v26 quad_perm:[2,3,0,1] row_mask:0xf bank_mask:0xf bound_ctrl:1
	s_nop 0
	v_add_f32_dpp v18, v18, v18 quad_perm:[1,0,3,2] row_mask:0xf bank_mask:0xf bound_ctrl:1
	v_add_f32_dpp v19, v19, v19 row_half_mirror row_mask:0xf bank_mask:0xf bound_ctrl:1
	s_nop 0
	v_add_f32_dpp v18, v18, v18 quad_perm:[2,3,0,1] row_mask:0xf bank_mask:0xf bound_ctrl:1
	v_add_f32_dpp v20, v19, v19 row_mirror row_mask:0xf bank_mask:0xf bound_ctrl:1
	s_nop 0
	v_add_f32_dpp v18, v18, v18 row_half_mirror row_mask:0xf bank_mask:0xf bound_ctrl:1
	s_nop 1
	v_add_f32_dpp v18, v18, v18 row_mirror row_mask:0xf bank_mask:0xf bound_ctrl:1
	v_fmamk_f32 v18, v18, 0x3c800000, v193
	v_rsq_f32_e32 v18, v18
	s_nop 0
	v_pk_mul_f32 v[14:15], v[14:15], v[18:19] op_sel_hi:[1,0]
	v_pk_mul_f32 v[16:17], v[16:17], v[18:19] op_sel_hi:[1,0]
	v_pk_fma_f32 v[14:15], v[2:3], v[14:15], v[6:7]
	v_pk_fma_f32 v[16:17], v[4:5], v[16:17], v[8:9]
	v_pk_fma_f32 v[14:15], v[20:21], v[22:23], v[14:15] op_sel_hi:[0,1,1]
	v_pk_fma_f32 v[16:17], v[20:21], v[24:25], v[16:17] op_sel_hi:[0,1,1]
	s_waitcnt vmcnt(1)
	v_lshlrev_b32_e32 v18, 16, v174
	v_and_b32_e32 v19, 0xffff0000, v174
	v_lshlrev_b32_e32 v20, 16, v175
	v_and_b32_e32 v21, 0xffff0000, v175
	v_pk_mul_f32 v[16:17], v[16:17], v[20:21]
	v_pk_mul_f32 v[14:15], v[14:15], v[18:19]
	s_nop 0
	v_cvt_pk_bf16_f32 v14, v14, v15
	v_cvt_pk_bf16_f32 v15, v16, v17
	v_lshl_or_b32 v16, s5, 4, v176
	v_or_b32_e32 v16, s6, v16
	v_mov_b32_e32 v17, s7
	v_lshlrev_b64 v[16:17], 12, v[16:17]
	v_lshl_add_u64 v[16:17], v[168:169], 0, v[16:17]
	global_store_dwordx2 v[16:17], v[14:15], off
	s_waitcnt lgkmcnt(0)
	s_and_saveexec_b64 s[12:13], s[2:3]
	v_mov_b32_e32 v14, s34
	v_mov_b32_e32 v15, 1
	ds_add_u32 v14, v15
	v_mov_b32_e32 v14, s31
	ds_add_u32 v14, v15

.LBB0_653:
	s_lshl_b32 s8, s16, 4
	v_lshl_add_u64 v[14:15], v[166:167], 0, s[8:9]
	v_mov_b64_e32 v[16:17], s[66:67]
	v_mad_u64_u32 v[16:17], s[14:15], v14, s36, v[16:17]
	v_mov_b32_e32 v14, v17
	v_mad_u64_u32 v[14:15], s[14:15], v15, s36, v[14:15]
	v_mov_b32_e32 v17, v14
	s_mov_b32 s5, s9
	v_lshl_add_u64 v[14:15], v[16:17], 0, s[4:5]
	v_lshl_add_u64 v[14:15], v[14:15], 0, v[162:163]
	v_add_co_u32_e32 v14, vcc, s37, v14
	v_cvt_pk_bf16_f32 v198, v106, v107
	s_nop 0
	v_addc_co_u32_e32 v15, vcc, 0, v15, vcc
	global_load_dwordx2 v[174:175], v[14:15], off
	v_cvt_pk_bf16_f32 v199, v108, v109
	v_cvt_pk_bf16_f32 v200, v110, v111
	v_cvt_pk_bf16_f32 v201, v112, v113
	v_cvt_pk_bf16_f32 v158, v114, v115
	v_cvt_pk_bf16_f32 v159, v116, v117
	v_mfma_f32_16x16x32_bf16 v[42:45], v[154:157], v[198:201], 0
	v_cvt_pk_bf16_f32 v160, v118, v119
	v_cvt_pk_bf16_f32 v161, v120, v121
	v_mov_b32_e32 v82, v84
	v_mov_b32_e32 v83, v85
	v_mfma_f32_16x16x32_bf16 v[42:45], v[146:149], v[158:161], v[42:45]
	s_mul_i32 s5, s16, 205
	s_lshr_b32 s5, s5, 10
	s_mul_i32 s5, s5, 5
	s_sub_i32 s5, s16, s5
	s_mul_i32 s5, s5, 14336
	s_add_i32 s8, s5, 0
	v_mfma_f32_16x16x32_bf16 v[42:45], v[150:153], v[82:85], v[42:45]
	v_add_u32_e32 v14, s8, v184
	v_add_u32_e32 v18, s8, v185
	v_add_u32_e32 v22, s8, v187
	v_add3_u32 v32, s8, v188, v183
	v_add_u32_e32 v146, s8, v186
	s_nop 2
	v_cvt_pk_bf16_f32 v42, v42, v43
	v_cvt_pk_bf16_f32 v43, v44, v45
	v_mov_b32_e32 v44, v163
	v_mov_b32_e32 v45, v163
	ds_read_b128 v[70:73], v14
	ds_read_b128 v[62:65], v14 offset:64
	ds_read_b128 v[58:61], v14 offset:2048
	ds_read_b128 v[14:17], v14 offset:2112
	ds_read_b128 v[74:77], v18 offset:4096
	ds_read_b128 v[66:69], v18 offset:5120
	ds_read_b128 v[38:41], v18 offset:6144
	ds_read_b128 v[34:37], v18 offset:7168
	ds_read_b128 v[26:29], v22 offset:8192
	ds_read_b128 v[18:21], v22 offset:9216
	ds_read_b128 v[22:25], v22 offset:10240
	ds_read_b64 v[32:33], v32 offset:11264
	v_mfma_f32_16x16x32_bf16 v[142:145], v[142:145], v[42:45], 0
	ds_read_b128 v[54:57], v146 offset:13312
	ds_read_b128 v[46:49], v146 offset:13376
	ds_read_b128 v[50:53], v146 offset:13440
	ds_read_b128 v[42:45], v146 offset:13504
	s_mov_b32 s5, 0
	v_mfma_f32_16x16x32_bf16 v[138:141], v[138:141], v[198:201], 0
	s_cmp_lt_u32 s43, s99
	s_cbranch_scc1 .Lscan_y2_skip
	s_branch .LBB0_655

; __global__ void __launch_bounds__(NTHR, 2) mk_fwd(Args args) {
;     ...
;                 CK_POST(B, NCHUNK - 1);
.LBB0_664:
	s_add_i32 s5, 0, 0x23000
	v_add3_u32 v14, s5, v30, v182
	s_add_i32 s5, 0, 0x2c00
	v_add3_u32 v25, s5, v181, v31
	ds_read_u16 v18, v25
	ds_read_u16 v19, v25 offset:32
	ds_read_u16 v20, v25 offset:64
	ds_read_b128 v[14:17], v14
	s_add_i32 s6, s35, 0
	s_waitcnt lgkmcnt(3)
	v_lshlrev_b32_e32 v22, 16, v18
	v_add_u32_e32 v18, 0, v180
	v_add_u32_e32 v1, 0, v1
	v_add_u32_e32 v26, 0x800, v18
	s_add_i32 s6, s6, 0x1c00
	v_add_u32_e32 v1, 0x3400, v1
	s_waitcnt lgkmcnt(2)
	v_lshlrev_b32_e32 v23, 16, v19
	s_waitcnt lgkmcnt(1)
	v_lshlrev_b32_e32 v24, 16, v20
	v_add3_u32 v28, s6, v178, v179
	ds_read_b128 v[18:21], v1
	ds_read_u16 v1, v25 offset:96
	ds_read_b64 v[26:27], v26
	ds_read_u16 v30, v28 offset:8
	ds_read_u16 v31, v28 offset:72
	ds_read_u16 v32, v28 offset:136
	ds_read_u16 v33, v28 offset:200
	s_waitcnt lgkmcnt(6)
	v_rcp_f32_e32 v18, v18
	v_rcp_f32_e32 v19, v19
	s_waitcnt lgkmcnt(4)
	v_lshlrev_b32_e32 v28, 16, v26
	v_and_b32_e32 v29, 0xffff0000, v26
	s_waitcnt lgkmcnt(2)
	v_lshlrev_b32_e32 v31, 16, v31
	v_lshlrev_b32_e32 v30, 16, v30
	v_pk_mul_f32 v[28:29], v[28:29], v[30:31]
	v_lshlrev_b32_e32 v25, 16, v1
	v_pk_mul_f32 v[10:11], v[10:11], v[28:29]
	s_waitcnt lgkmcnt(1)
	v_lshlrev_b32_e32 v26, 16, v32
	v_pk_mul_f32 v[10:11], v[18:19], v[10:11]
	v_rcp_f32_e32 v18, v20
	v_add_f32_e32 v1, v10, v11
	v_add_f32_e32 v10, v14, v15
	v_rcp_f32_e32 v19, v21
	v_add_f32_e32 v10, v16, v10
	v_lshlrev_b32_e32 v20, 16, v27
	v_and_b32_e32 v21, 0xffff0000, v27
	s_waitcnt lgkmcnt(0)
	v_lshlrev_b32_e32 v27, 16, v33
	v_add_f32_e32 v10, v17, v10
	v_pk_mul_f32 v[20:21], v[20:21], v[26:27]
	v_or_b32_e32 v164, 0xff0000, v164
	v_add_f32_dpp v10, v10, v10 quad_perm:[1,0,3,2] row_mask:0xf bank_mask:0xf bound_ctrl:1
	v_pk_mul_f32 v[12:13], v[12:13], v[20:21]
	s_mov_b32 s5, 0
	v_add_f32_dpp v10, v10, v10 quad_perm:[2,3,0,1] row_mask:0xf bank_mask:0xf bound_ctrl:1
	v_pk_mul_f32 v[12:13], v[18:19], v[12:13]
	v_mov_b32_e32 v163, 0
	v_add_f32_dpp v10, v10, v10 row_half_mirror row_mask:0xf bank_mask:0xf bound_ctrl:1
	v_add_f32_e32 v1, v1, v12
	v_add_f32_e32 v1, v1, v13
	v_add_f32_dpp v12, v10, v10 row_mirror row_mask:0xf bank_mask:0xf bound_ctrl:1
	v_fmamk_f32 v11, v12, 0xbc800000, v15
	v_fmamk_f32 v10, v12, 0xbc800000, v14
	v_fmamk_f32 v17, v12, 0xbc800000, v17
	v_fmac_f32_e32 v16, 0xbc800000, v12
	v_pk_mul_f32 v[14:15], v[10:11], v[10:11]
	v_pk_mul_f32 v[12:13], v[16:17], v[16:17]
	v_add_f32_e32 v14, v14, v15
	v_add_f32_e32 v12, v12, v14
	v_add_f32_e32 v12, v13, v12
	v_mov_b32_e32 v13, 0x3a27c5ac
	v_add_f32_dpp v1, v1, v1 quad_perm:[1,0,3,2] row_mask:0xf bank_mask:0xf bound_ctrl:1
	v_add_f32_dpp v12, v12, v12 quad_perm:[1,0,3,2] row_mask:0xf bank_mask:0xf bound_ctrl:1
	s_nop 0
	v_add_f32_dpp v1, v1, v1 quad_perm:[2,3,0,1] row_mask:0xf bank_mask:0xf bound_ctrl:1
	v_add_f32_dpp v12, v12, v12 quad_perm:[2,3,0,1] row_mask:0xf bank_mask:0xf bound_ctrl:1
	s_nop 0
	v_add_f32_dpp v1, v1, v1 row_half_mirror row_mask:0xf bank_mask:0xf bound_ctrl:1
	v_add_f32_dpp v12, v12, v12 row_half_mirror row_mask:0xf bank_mask:0xf bound_ctrl:1
	s_nop 0
	v_add_f32_dpp v14, v1, v1 row_mirror row_mask:0xf bank_mask:0xf bound_ctrl:1
	v_add_f32_dpp v12, v12, v12 row_mirror row_mask:0xf bank_mask:0xf bound_ctrl:1
	v_fmac_f32_e32 v13, 0x3c800000, v12
	v_rsq_f32_e32 v12, v13
	s_nop 0
	v_pk_mul_f32 v[10:11], v[10:11], v[12:13] op_sel_hi:[1,0]
	v_pk_mul_f32 v[12:13], v[16:17], v[12:13] op_sel_hi:[1,0]
	v_pk_fma_f32 v[2:3], v[2:3], v[10:11], v[6:7]
	v_pk_fma_f32 v[4:5], v[4:5], v[12:13], v[8:9]
	v_pk_fma_f32 v[2:3], v[14:15], v[22:23], v[2:3] op_sel_hi:[0,1,1]
	v_pk_fma_f32 v[4:5], v[14:15], v[24:25], v[4:5] op_sel_hi:[0,1,1]
	s_waitcnt vmcnt(2)
	v_lshlrev_b32_e32 v6, 16, v172
	v_and_b32_e32 v7, 0xffff0000, v172
	v_lshlrev_b32_e32 v8, 16, v173
	v_and_b32_e32 v9, 0xffff0000, v173
	v_pk_mul_f32 v[4:5], v[4:5], v[8:9]
	v_pk_mul_f32 v[2:3], v[2:3], v[6:7]
	s_nop 0
	v_cvt_pk_bf16_f32 v2, v2, v3
	v_cvt_pk_bf16_f32 v3, v4, v5
	v_lshl_add_u64 v[4:5], s[62:63], 0, v[164:165]
	v_lshl_add_u64 v[4:5], v[4:5], 0, s[4:5]
	v_lshl_add_u64 v[4:5], v[4:5], 0, v[162:163]
	global_store_dwordx2 v[4:5], v[2:3], off
	s_waitcnt lgkmcnt(0)
	s_and_saveexec_b64 s[4:5], s[2:3]
	s_cbranch_execz .LBB0_669
	s_mov_b64 s[6:7], exec
	v_mbcnt_lo_u32_b32 v1, s6, 0
	v_mbcnt_hi_u32_b32 v1, s7, v1
	v_cmp_eq_u32_e32 vcc, 0, v1
	s_and_saveexec_b64 s[2:3], vcc
	s_bcnt1_i32_b64 s6, s[6:7]
	v_mov_b32_e32 v1, s34
	v_mov_b32_e32 v2, s6
	ds_add_u32 v1, v2
	s_or_b64 exec, exec, s[2:3]
	s_mov_b64 s[2:3], exec
	v_mbcnt_lo_u32_b32 v1, s2, 0
	v_mbcnt_hi_u32_b32 v1, s3, v1
	v_cmp_eq_u32_e32 vcc, 0, v1
	s_and_b64 s[6:7], exec, vcc
	s_mov_b64 exec, s[6:7]
	s_bcnt1_i32_b64 s2, s[2:3]
	v_mov_b32_e32 v1, s31
	v_mov_b32_e32 v2, s2
	ds_add_u32 v1, v2

; #define LAS __attribute__((address_space(3)))
; __global__ void __launch_bounds__(NTHR, 2) mk_fwd(Args args) {
;     ...
;                 const int j = lane;
;                 LAS bf16* IMG = (LAS bf16*)(lds + wave * 13312);
;                 LAS bf16* QGT = (LAS bf16*)(lds + wave * 13312 + 10240);
;                 for (int i = lane; i < 768; i += 64) ((LAS unsigned*)QGT)[i] = 0u;
;                 const int pos = (j & 32) | ((j & 12) << 1) | ((j & 16) >> 2) | (j & 3);
;                 bf16 nr_[17], nk_[17], nv_[17], nwl_[16], nal_[16]; float ncst_[7];
;     ...
;                 if (gw < 64 * NCHUNK) P4_FETCH(gw);
.Lprod_code:
	v_readlane_b32 s0, v252, 43
	s_nop 3
	s_sub_i32 s0, s0, 4
	s_mulk_i32 s0, 0x3400
	s_add_i32 s4, s0, 0x11800
	s_mov_b32 s77, 0
	s_cmpk_gt_i32 s30, 0x3fff
	v_lshl_add_u32 v125, v194, 2, s4
	v_mov_b32_e32 v7, 0
	ds_write2st64_b32 v125, v7, v7 offset0:40 offset1:41
	ds_write2st64_b32 v125, v7, v7 offset0:42 offset1:43
	ds_write2st64_b32 v125, v7, v7 offset0:44 offset1:45
	ds_write2st64_b32 v125, v7, v7 offset0:46 offset1:47
	ds_write2st64_b32 v125, v7, v7 offset0:48 offset1:49
	ds_write2st64_b32 v125, v7, v7 offset0:50 offset1:51
	s_cbranch_scc1 .Lprod_exit
	v_writelane_b32 v252, s2, 52
	s_ashr_i32 s0, s30, 12
	s_lshl_b32 s5, s30, 6
	v_writelane_b32 v252, s3, 53
	s_bfe_u32 s2, s30, 0x80004
	s_ashr_i32 s1, s0, 31
	s_lshl_b32 s3, s2, 4
	s_and_b32 s5, s5, 0x3c0
	s_add_u32 s29, s26, 0x21c08000
	s_addc_u32 s31, s27, 0
	s_lshl_b32 s8, s5, 1
	s_add_u32 s6, s66, s8
	s_addc_u32 s7, s67, 0
	s_add_u32 s8, s10, s8
	s_addc_u32 s9, s11, 0
	s_lshl_b64 s[12:13], s[0:1], 12
	v_lshlrev_b32_e32 v1, 1, v0
	v_lshrrev_b32_e32 v2, 2, v0
	s_or_b32 s0, s12, s3
	v_and_b32_e32 v92, 15, v0
	v_and_b32_e32 v1, 24, v1
	v_and_b32_e32 v2, 4, v2
	v_and_b32_e32 v4, 3, v0
	v_and_b32_e32 v3, 35, v0
	s_add_u32 s1, s0, -1
	v_lshlrev_b32_e32 v5, 3, v0
	v_or3_b32 v101, v3, v2, v1
	s_addc_u32 s14, s13, -1
	v_and_b32_e32 v97, 56, v5
	v_mul_u32_u24_e32 v5, 0x48, v92
	v_lshlrev_b32_e32 v1, 1, v1
	v_lshlrev_b32_e32 v4, 1, v4
	s_cmp_eq_u32 s2, 0
	v_lshlrev_b32_e32 v5, 1, v5
	v_add3_u32 v1, s4, v1, v4
	v_lshlrev_b32_e32 v18, 1, v194
	v_mov_b32_e32 v19, v7
	v_and_b32_e32 v4, 48, v194
	v_lshl_add_u64 v[14:15], s[10:11], 0, v[18:19]
	v_lshl_add_u64 v[16:17], s[66:67], 0, v[18:19]
	v_add3_u32 v98, s4, v5, v4
	v_lshl_add_u64 v[4:5], s[6:7], 0, v[18:19]
	v_lshl_add_u64 v[18:19], s[8:9], 0, v[18:19]
	s_cselect_b32 s1, s12, s1
	s_cselect_b32 s6, s13, s14
	v_mov_b32_e32 v99, 0x2400
	s_mul_i32 s8, s6, 0x2400
	v_mad_u64_u32 v[22:23], s[6:7], s1, v99, v[18:19]
	v_add_u32_e32 v23, s8, v23
	s_movk_i32 s36, 0x1000
	global_load_ushort v24, v[22:23], off
	global_load_ushort v21, v[22:23], off offset:2048
	v_add_co_u32_e32 v22, vcc, s36, v22
	v_mad_i64_i32 v[18:19], s[6:7], s0, v99, v[18:19]
	s_nop 0
	v_addc_co_u32_e32 v23, vcc, 0, v23, vcc
	v_add_co_u32_e32 v26, vcc, s36, v18
	s_movk_i32 s37, 0x2000
	s_nop 0
	v_addc_co_u32_e32 v27, vcc, 0, v19, vcc
	global_load_ushort v20, v[22:23], off
	global_load_ushort v25, v[18:19], off
	s_nop 0
	global_load_ushort v22, v[18:19], off offset:2048
	global_load_ushort v23, v[26:27], off
	s_mov_b64 s[6:7], 0x2400
	v_add_co_u32_e32 v26, vcc, s37, v18
	v_lshl_add_u64 v[28:29], v[18:19], 0, s[6:7]
	s_nop 0
	v_addc_co_u32_e32 v27, vcc, 0, v19, vcc
	s_movk_i32 s38, 0x3000
	global_load_ushort v27, v[26:27], off offset:1024
	s_nop 0
	global_load_ushort v26, v[28:29], off offset:2048
	v_add_co_u32_e32 v28, vcc, s38, v18
	s_movk_i32 s8, 0x4000
	s_nop 0
	v_addc_co_u32_e32 v29, vcc, 0, v19, vcc
	global_load_ushort v96, v[28:29], off offset:1024
	v_add_co_u32_e32 v28, vcc, s8, v18
	s_movk_i32 s1, 0x5000
	s_nop 0
	v_addc_co_u32_e32 v29, vcc, 0, v19, vcc
	s_mov_b64 s[6:7], 0x4800
	v_add_co_u32_e32 v32, vcc, s1, v18
	v_lshl_add_u64 v[30:31], v[18:19], 0, s[6:7]
	s_nop 0
	v_addc_co_u32_e32 v33, vcc, 0, v19, vcc
	s_movk_i32 s9, 0x6000
	global_load_ushort v29, v[28:29], off offset:2048
	s_nop 0
	global_load_ushort v30, v[30:31], off offset:2048
	s_mov_b64 s[10:11], 0x6c00
	global_load_ushort v121, v[32:33], off offset:2048
	v_add_co_u32_e32 v32, vcc, s9, v18
	v_lshl_add_u64 v[34:35], v[18:19], 0, s[10:11]
	s_nop 0
	v_addc_co_u32_e32 v33, vcc, 0, v19, vcc
	s_movk_i32 s42, 0x7000
	global_load_ushort v32, v[32:33], off offset:3072
	s_nop 0
	global_load_ushort v31, v[34:35], off offset:2048
	v_add_co_u32_e32 v34, vcc, s42, v18
	s_mov_b32 s44, 0xa000
	s_nop 0
	v_addc_co_u32_e32 v35, vcc, 0, v19, vcc
	s_mov_b64 s[10:11], 0x9000
	v_add_co_u32_e32 v36, vcc, s44, v18
	global_load_ushort v122, v[34:35], off offset:3072
	v_lshl_add_u64 v[34:35], v[18:19], 0, s[10:11]
	v_addc_co_u32_e32 v37, vcc, 0, v19, vcc
	s_mov_b32 s1, 0xb000
	global_load_ushort v33, v[36:37], off offset:-4096
	s_nop 0
	global_load_ushort v34, v[34:35], off offset:2048
	s_nop 0
	global_load_ushort v123, v[36:37], off
	s_mov_b64 s[14:15], 0xb400
	v_add_co_u32_e32 v36, vcc, s1, v18
	v_lshl_add_u64 v[38:39], v[18:19], 0, s[14:15]
	s_nop 0
	v_addc_co_u32_e32 v37, vcc, 0, v19, vcc
	s_mov_b32 s39, 0xc000
	global_load_ushort v36, v[36:37], off offset:1024
	s_nop 0
	global_load_ushort v35, v[38:39], off offset:2048
	v_add_co_u32_e32 v38, vcc, s39, v18
	s_mov_b32 s41, 0xd000
	s_nop 0
	v_addc_co_u32_e32 v39, vcc, 0, v19, vcc
	global_load_ushort v124, v[38:39], off offset:1024
	s_mov_b64 s[14:15], 0xd800
	v_add_co_u32_e32 v38, vcc, s41, v18
	v_lshl_add_u64 v[40:41], v[18:19], 0, s[14:15]
	s_nop 0
	v_addc_co_u32_e32 v39, vcc, 0, v19, vcc
	s_mov_b32 s1, 0xe000
	global_load_ushort v38, v[38:39], off offset:2048
	s_nop 0
	global_load_ushort v37, v[40:41], off offset:2048
	v_add_co_u32_e32 v40, vcc, s1, v18
	s_mov_b32 s49, 0xf000
	s_nop 0
	v_addc_co_u32_e32 v41, vcc, 0, v19, vcc
	s_mov_b64 s[16:17], 0xfc00
	v_add_co_u32_e32 v42, vcc, s49, v18
	global_load_ushort v127, v[40:41], off offset:2048
	v_lshl_add_u64 v[40:41], v[18:19], 0, s[16:17]
	v_addc_co_u32_e32 v43, vcc, 0, v19, vcc
	s_mov_b32 s50, 0x10000
	global_load_ushort v43, v[42:43], off offset:3072
	s_nop 0
	global_load_ushort v39, v[40:41], off offset:2048
	v_add_co_u32_e32 v40, vcc, s50, v18
	s_mov_b32 s73, 0x13000
	s_nop 0
	v_addc_co_u32_e32 v41, vcc, 0, v19, vcc
	s_mov_b64 s[46:47], 0x12000
	v_add_co_u32_e32 v46, vcc, s73, v18
	global_load_ushort v128, v[40:41], off offset:3072
	v_lshl_add_u64 v[40:41], v[18:19], 0, s[46:47]
	v_addc_co_u32_e32 v47, vcc, 0, v19, vcc
	s_mov_b32 s1, 0x14000
	global_load_ushort v45, v[46:47], off offset:-4096
	global_load_ushort v44, v[40:41], off offset:2048
	s_nop 0
	global_load_ushort v41, v[46:47], off
	s_mov_b64 s[16:17], 0x14400
	v_add_co_u32_e32 v46, vcc, s1, v18
	v_lshl_add_u64 v[48:49], v[18:19], 0, s[16:17]
	s_nop 0
	v_addc_co_u32_e32 v47, vcc, 0, v19, vcc
	s_mov_b32 s78, 0x15000
	global_load_ushort v47, v[46:47], off offset:1024
	s_nop 0
	global_load_ushort v46, v[48:49], off offset:2048
	v_add_co_u32_e32 v48, vcc, s78, v18
	s_mov_b32 s72, 0x16000
	s_nop 0
	v_addc_co_u32_e32 v49, vcc, 0, v19, vcc
	global_load_ushort v129, v[48:49], off offset:1024
	s_mov_b64 s[16:17], 0x16800
	v_add_co_u32_e32 v48, vcc, s72, v18
	v_lshl_add_u64 v[50:51], v[18:19], 0, s[16:17]
	s_nop 0
	v_addc_co_u32_e32 v49, vcc, 0, v19, vcc
	s_mov_b32 s1, 0x17000
	global_load_ushort v49, v[48:49], off offset:2048
	s_nop 0
	global_load_ushort v48, v[50:51], off offset:2048
	v_add_co_u32_e32 v50, vcc, s1, v18
	s_mov_b32 s1, 0x18000
	s_nop 0
	v_addc_co_u32_e32 v51, vcc, 0, v19, vcc
	global_load_ushort v130, v[50:51], off offset:2048
	s_mov_b64 s[34:35], 0x18c00
	v_add_co_u32_e32 v50, vcc, s1, v18
	v_lshl_add_u64 v[52:53], v[18:19], 0, s[34:35]
	s_nop 0
	v_addc_co_u32_e32 v51, vcc, 0, v19, vcc
	s_mov_b32 s1, 0x19000
	global_load_ushort v51, v[50:51], off offset:3072
	s_nop 0
	global_load_ushort v50, v[52:53], off offset:2048
	v_add_co_u32_e32 v52, vcc, s1, v18
	s_mov_b32 s1, 0x1c000
	s_nop 0
	v_addc_co_u32_e32 v53, vcc, 0, v19, vcc
	s_mov_b64 s[34:35], 0x1b000
	v_add_co_u32_e32 v56, vcc, s1, v18
	v_lshl_add_u64 v[54:55], v[18:19], 0, s[34:35]
	s_nop 0
	v_addc_co_u32_e32 v57, vcc, 0, v19, vcc
	s_mov_b32 s1, 0x1d000
	global_load_ushort v133, v[52:53], off offset:3072
	s_nop 0
	global_load_ushort v53, v[56:57], off offset:-4096
	global_load_ushort v52, v[54:55], off offset:2048
	global_load_ushort v134, v[56:57], off
	s_mov_b64 s[34:35], 0x1d400
	v_add_co_u32_e32 v54, vcc, s1, v18
	v_lshl_add_u64 v[56:57], v[18:19], 0, s[34:35]
	s_nop 0
	v_addc_co_u32_e32 v55, vcc, 0, v19, vcc
	s_mov_b32 s1, 0x1e000
	global_load_ushort v55, v[54:55], off offset:1024
	s_nop 0
	global_load_ushort v54, v[56:57], off offset:2048
	v_add_co_u32_e32 v56, vcc, s1, v18
	s_mov_b32 s1, 0x1f000
	s_nop 0
	v_addc_co_u32_e32 v57, vcc, 0, v19, vcc
	v_add_co_u32_e32 v58, vcc, s1, v18
	s_mov_b32 s1, 0x20000
	s_nop 0
	v_addc_co_u32_e32 v59, vcc, 0, v19, vcc
	v_add_co_u32_e32 v60, vcc, s1, v18
	s_mov_b32 s1, 0x21000
	s_nop 0
	v_addc_co_u32_e32 v61, vcc, 0, v19, vcc
	s_mov_b64 s[34:35], 0x1f800
	v_add_co_u32_e32 v62, vcc, s1, v18
	global_load_ushort v135, v[56:57], off offset:1024
	v_lshl_add_u64 v[56:57], v[18:19], 0, s[34:35]
	s_mov_b64 s[34:35], 0x21c00
	v_addc_co_u32_e32 v63, vcc, 0, v19, vcc
	s_mov_b32 s1, 0x22000
	global_load_ushort v59, v[58:59], off offset:2048
	s_nop 0
	global_load_ushort v56, v[56:57], off offset:2048
	v_mov_b32_e32 v100, 0x1800
	global_load_ushort v136, v[60:61], off offset:2048
	v_lshl_add_u64 v[60:61], v[18:19], 0, s[34:35]
	v_add_co_u32_e32 v18, vcc, s1, v18
	v_mad_i64_i32 v[4:5], s[0:1], s0, v100, v[4:5]
	s_nop 0
	v_addc_co_u32_e32 v19, vcc, 0, v19, vcc
	global_load_ushort v64, v[62:63], off offset:3072
	s_nop 0
	global_load_ushort v61, v[60:61], off offset:2048
	v_add_co_u32_e32 v62, vcc, s36, v4
	s_mov_b64 s[0:1], 0x1800
	s_nop 0
	v_addc_co_u32_e32 v63, vcc, 0, v5, vcc
	v_add_co_u32_e32 v66, vcc, s38, v4
	global_load_ushort v137, v[18:19], off offset:3072
	v_lshl_add_u64 v[18:19], v[4:5], 0, s[0:1]
	s_mov_b64 s[0:1], 0x3000
	v_addc_co_u32_e32 v67, vcc, 0, v5, vcc
	global_load_ushort v58, v[4:5], off
	global_load_ushort v57, v[4:5], off offset:2048
	s_nop 0
	global_load_ushort v62, v[62:63], off offset:2048
	s_nop 0
	global_load_ushort v60, v[18:19], off offset:2048
	v_lshl_add_u64 v[18:19], v[4:5], 0, s[0:1]
	global_load_ushort v65, v[66:67], off
	global_load_ushort v63, v[18:19], off offset:2048
	v_add_co_u32_e32 v66, vcc, s8, v4
	s_mov_b32 s12, 0x9000
	s_nop 0
	v_addc_co_u32_e32 v67, vcc, 0, v5, vcc
	v_add_co_u32_e32 v68, vcc, s9, v4
	v_lshl_add_u64 v[18:19], v[4:5], 0, s[6:7]
	s_nop 0
	v_addc_co_u32_e32 v69, vcc, 0, v5, vcc
	v_add_co_u32_e32 v70, vcc, s42, v4
	s_mov_b64 s[0:1], 0x6000
	s_nop 0
	v_addc_co_u32_e32 v71, vcc, 0, v5, vcc
	v_add_co_u32_e32 v72, vcc, s12, v4
	global_load_ushort v67, v[66:67], off offset:2048
	s_nop 0
	global_load_ushort v66, v[18:19], off offset:2048
	v_addc_co_u32_e32 v73, vcc, 0, v5, vcc
	v_add_co_u32_e32 v74, vcc, s44, v4
	v_lshl_add_u64 v[18:19], v[4:5], 0, s[0:1]
	s_nop 0
	v_addc_co_u32_e32 v75, vcc, 0, v5, vcc
	v_add_co_u32_e32 v76, vcc, s39, v4
	s_mov_b64 s[0:1], 0x7800
	s_nop 0
	v_addc_co_u32_e32 v77, vcc, 0, v5, vcc
	v_add_co_u32_e32 v78, vcc, s41, v4
	global_load_ushort v69, v[68:69], off
	s_nop 0
	global_load_ushort v68, v[18:19], off offset:2048
	v_addc_co_u32_e32 v79, vcc, 0, v5, vcc
	v_lshl_add_u64 v[18:19], v[4:5], 0, s[0:1]
	v_add_co_u32_e32 v80, vcc, s49, v4
	global_load_ushort v71, v[70:71], off offset:2048
	s_nop 0
	global_load_ushort v70, v[18:19], off offset:2048
	v_lshl_add_u64 v[18:19], v[4:5], 0, s[10:11]
	s_mov_b64 s[0:1], 0xa800
	v_addc_co_u32_e32 v81, vcc, 0, v5, vcc
	global_load_ushort v73, v[72:73], off
	s_nop 0
	global_load_ushort v72, v[18:19], off offset:2048
	v_lshl_add_u64 v[18:19], v[4:5], 0, s[0:1]
	s_mov_b64 s[0:1], 0xc000
	v_add_co_u32_e32 v82, vcc, s50, v4
	s_mov_b32 s13, 0x12000
	global_load_ushort v75, v[74:75], off offset:2048
	s_nop 0
	global_load_ushort v74, v[18:19], off offset:2048
	v_lshl_add_u64 v[18:19], v[4:5], 0, s[0:1]
; __device__ __forceinline__ unsigned f2bf(float f) { return cvt_pk_bf16_nat(f, 0.f) & 0xffffu; }
; __global__ void __launch_bounds__(NTHR, 2) mk_fwd(Args args) {
;     ...
;                 if (gw < 64 * NCHUNK) P4_FETCH(gw);
;     ...
;                     const int s_ = tr, rec = (s_ >> 2) * 8 + (s_ & 3);
; #pragma unroll
;                     for (int e = 0; e < 4; ++e) { const int t = 4 * q + e;
;                         const float qv = s_ < t ? QT[e] : 0.f, gb = s_ <= t ? GB[e] : 0.f, gk = s_ <= t ? GK[e] : 0.f;
;                         QGT[t * 32 + rec] = (bf16)f2bf(qv);
;                         QGT[512 + t * 32 + rec] = (bf16)f2bf(gb); QGT[512 + t * 32 + rec + 4] = (bf16)f2bf(gk); }
;                     float Tr[16]; const pg8::v4i_t PTi = __builtin_bit_cast(pg8::v4i_t, PT);
; #pragma unroll
;                     for (int t = 0; t < 16; ++t) { float acc = (t == s_) ? 1.f : 0.f;
	v_addc_co_u32_e32 v83, vcc, 0, v5, vcc
	global_load_ushort v77, v[76:77], off
	s_nop 0
	global_load_ushort v76, v[18:19], off offset:2048
	v_lshl_add_u64 v[18:19], v[4:5], 0, s[14:15]
	s_mov_b64 s[0:1], 0xf000
	v_add_co_u32_e32 v84, vcc, s13, v4
	global_load_ushort v79, v[78:79], off offset:2048
	s_nop 0
	global_load_ushort v78, v[18:19], off offset:2048
	v_lshl_add_u64 v[18:19], v[4:5], 0, s[0:1]
	s_mov_b64 s[0:1], 0x10800
	v_addc_co_u32_e32 v85, vcc, 0, v5, vcc
	global_load_ushort v81, v[80:81], off
	s_nop 0
	global_load_ushort v80, v[18:19], off offset:2048
	v_lshl_add_u64 v[18:19], v[4:5], 0, s[0:1]
	v_add_co_u32_e32 v86, vcc, s73, v4
	global_load_ushort v83, v[82:83], off offset:2048
	s_nop 0
	global_load_ushort v82, v[18:19], off offset:2048
	v_lshl_add_u64 v[18:19], v[4:5], 0, s[46:47]
	s_mov_b64 s[0:1], 0x13800
	v_addc_co_u32_e32 v87, vcc, 0, v5, vcc
	global_load_ushort v85, v[84:85], off
	s_nop 0
	global_load_ushort v84, v[18:19], off offset:2048
	v_lshl_add_u64 v[18:19], v[4:5], 0, s[0:1]
	s_mov_b64 s[0:1], 0x15000
	v_add_co_u32_e32 v88, vcc, s78, v4
	v_or_b32_e32 v2, s5, v194
	v_readlane_b32 s80, v252, 0
	global_load_ushort v87, v[86:87], off offset:2048
	s_nop 0
	global_load_ushort v86, v[18:19], off offset:2048
	v_lshl_add_u64 v[18:19], v[4:5], 0, s[0:1]
	v_addc_co_u32_e32 v89, vcc, 0, v5, vcc
	v_lshlrev_b32_e32 v6, 2, v2
	v_readlane_b32 s84, v252, 4
	v_readlane_b32 s85, v252, 5
	global_load_ushort v89, v[88:89], off
	s_nop 0
	global_load_ushort v88, v[18:19], off offset:2048
	v_lshl_add_u64 v[18:19], v[4:5], 0, s[16:17]
	v_add_co_u32_e32 v4, vcc, s72, v4
	v_lshl_add_u64 v[2:3], s[84:85], 0, v[6:7]
	s_nop 0
	v_addc_co_u32_e32 v5, vcc, 0, v5, vcc
	v_add_co_u32_e32 v2, vcc, s37, v2
	v_readlane_b32 s86, v252, 6
	s_nop 0
	v_addc_co_u32_e32 v3, vcc, 0, v3, vcc
	v_readlane_b32 s87, v252, 7
	v_readlane_b32 s90, v252, 10
	v_readlane_b32 s91, v252, 11
	global_load_ushort v91, v[4:5], off offset:2048
	global_load_ushort v90, v[18:19], off offset:2048
	global_load_dword v40, v6, s[84:85]
	global_load_dword v42, v[2:3], off offset:-4096
	s_nop 0
	global_load_dword v2, v[2:3], off
	s_nop 0
	global_load_dword v95, v6, s[86:87]
	global_load_dword v94, v6, s[90:91]
	global_load_dword v28, v6, s[52:53]
	global_load_dword v3, v6, s[54:55]
	s_movk_i32 s5, 0x48
	v_lshrrev_b32_e32 v4, 3, v194
	v_mad_u32_u24 v4, v4, s5, v97
	v_lshrrev_b32_e32 v93, 4, v194
	v_lshl_add_u32 v102, v4, 1, s4
	v_or_b32_e32 v4, 64, v194
	v_lshlrev_b32_e32 v104, 2, v93
	v_lshrrev_b32_e32 v5, 3, v4
	v_mad_u32_u24 v5, v5, s5, v97
	v_or_b32_e32 v6, 2, v104
	v_cmp_eq_u32_e32 vcc, 0, v92
	v_lshl_add_u32 v101, v101, 1, s4
	v_lshl_add_u32 v103, v5, 1, s4
	v_cmp_lt_u32_e64 s[4:5], v92, v104
	v_cmp_gt_u32_e64 s[6:7], v92, v104
	v_or_b32_e32 v5, 1, v104
	v_cmp_lt_u32_e64 s[10:11], v92, v6
	v_cmp_gt_u32_e64 s[12:13], v92, v6
	v_lshlrev_b32_e32 v131, 6, v6
	v_or_b32_e32 v6, 3, v104
	v_cndmask_b32_e64 v104, 0, 1.0, vcc
	v_cmp_eq_u32_e32 vcc, 1, v92
	v_cvt_pk_bf16_f32 v120, v104, s0
	v_readlane_b32 s0, v252, 40
	v_cndmask_b32_e64 v105, 0, 1.0, vcc
	v_cmp_eq_u32_e32 vcc, 2, v92
	s_lshl_b32 s0, s0, 3
	v_readlane_b32 s1, v252, 43
	v_cndmask_b32_e64 v106, 0, 1.0, vcc
	v_cmp_eq_u32_e32 vcc, 3, v92
	s_add_i32 s0, s1, s0
	s_mov_b32 s45, 0x5040100
	v_cndmask_b32_e64 v107, 0, 1.0, vcc
	v_cmp_eq_u32_e32 vcc, 4, v92
	s_add_i32 s34, s0, s28
	v_readlane_b32 s0, v252, 37
	v_cndmask_b32_e64 v108, 0, 1.0, vcc
	v_cmp_eq_u32_e32 vcc, 5, v92
	v_mul_u32_u24_e32 v126, 12, v194
	v_lshlrev_b32_e32 v18, 4, v4
	v_cndmask_b32_e64 v109, 0, 1.0, vcc
	v_cmp_eq_u32_e32 vcc, 6, v92
	v_lshlrev_b32_e32 v4, 8, v93
	v_cmp_gt_u32_e64 s[8:9], v92, v5
	v_cndmask_b32_e64 v110, 0, 1.0, vcc
	v_cmp_eq_u32_e32 vcc, 7, v92
	v_lshlrev_b32_e32 v5, 6, v5
	v_cmp_lt_u32_e64 s[14:15], v92, v6
	v_cndmask_b32_e64 v111, 0, 1.0, vcc
	v_cmp_eq_u32_e32 vcc, 8, v92
	v_cmp_gt_u32_e64 s[16:17], v92, v6
	v_lshlrev_b32_e32 v132, 6, v6
	v_cndmask_b32_e64 v112, 0, 1.0, vcc
	v_cmp_eq_u32_e32 vcc, 9, v92
	s_waitcnt vmcnt(0)
; __global__ void __launch_bounds__(NTHR, 2) mk_fwd(Args args) {
;     ...
;                 if (gw < 64 * NCHUNK) P4_FETCH(gw);
; #pragma unroll 1
;                 for (int u = gw; u < 64 * NCHUNK; u += NGW) {
;                     const int h = u & 15, c = (u >> 4) & 255, b = u >> 12, hd = b * 16 + h;
;                     const float mu_r = ncst_[0], mu_k = ncst_[1], mu_v = ncst_[2], c_w0 = ncst_[3], c_a0 = ncst_[4], c_kk = ncst_[5], c_ka = ncst_[6];
;                     unsigned char* pk = ws + WS_R + ((size_t)hd * NCHUNK + c) * PK_BYTES;
;                     float At[16], Rt[16], Bt[16], Kt[16], Vt[16];
;                     float xr_[17], xk_[17], xv_[17], xwl_[16], xal_[16];
; #pragma unroll
;                     for (int t = 0; t < 17; ++t) { xr_[t] = __builtin_bit_cast(float, (unsigned)nr_[t] << 16); xk_[t] = __builtin_bit_cast(float, (unsigned)nk_[t] << 16); xv_[t] = __builtin_bit_cast(float, (unsigned)nv_[t] << 16); }
; #pragma unroll
;                     for (int t = 0; t < 16; ++t) { xwl_[t] = __builtin_bit_cast(float, (unsigned)nwl_[t] << 16); xal_[t] = __builtin_bit_cast(float, (unsigned)nal_[t] << 16); }
;                     if (c == 0) { xr_[0] = 0.f; xk_[0] = 0.f; xv_[0] = 0.f; }
	v_perm_b32 v212, v127, v124, s45
	v_perm_b32 v213, v128, v127, s45
	v_cndmask_b32_e64 v113, 0, 1.0, vcc
	v_cmp_eq_u32_e32 vcc, 10, v92
	v_perm_b32 v214, v123, v122, s45
	v_perm_b32 v215, v121, v96, s45
	v_cndmask_b32_e64 v114, 0, 1.0, vcc
	v_cmp_eq_u32_e32 vcc, 11, v92
	v_perm_b32 v93, v137, v136, s45
	v_perm_b32 v96, v134, v133, s45
	v_cndmask_b32_e64 v115, 0, 1.0, vcc
	v_cmp_eq_u32_e32 vcc, 12, v92
	v_perm_b32 v97, v130, v129, s45
	s_add_i32 s34, s30, s28
	v_cndmask_b32_e64 v116, 0, 1.0, vcc
	v_cmp_eq_u32_e32 vcc, 13, v92
	v_lshlrev_b32_e32 v8, 6, v194
	v_lshlrev_b32_e32 v10, 5, v194
	v_cndmask_b32_e64 v117, 0, 1.0, vcc
	v_cmp_eq_u32_e32 vcc, 14, v92
	v_mov_b32_e32 v11, v7
	v_cmp_gt_u32_e64 s[2:3], 16, v194
	v_cndmask_b32_e64 v118, 0, 1.0, vcc
	v_cmp_eq_u32_e32 vcc, 15, v92
	v_perm_b32 v92, v136, v135, s45
	v_lshlrev_b32_e32 v12, 4, v194
	v_mov_b32_e32 v9, v7
	v_mov_b32_e32 v13, v7
	v_mov_b32_e32 v19, v7
	v_cndmask_b32_e64 v119, 0, 1.0, vcc
	s_lshl_b32 s48, s34, 6
	s_lshl_b32 s51, s28, 6
	s_mov_b32 s79, 0xbfb8aa3b
	v_lshlrev_b32_e32 v6, 2, v194
	v_add_u32_e32 v121, v1, v4
	v_add_u32_e32 v122, v1, v5
	v_add_u32_e32 v123, v1, v131
	v_add_u32_e32 v124, v1, v132
	v_add_u32_e32 v125, v125, v126
	s_mov_b32 s34, s30
	v_mov_b32_e32 v160, v57
	v_mov_b32_e32 v163, v60
	v_mov_b32_e32 v166, v63
	v_mov_b32_e32 v169, v66
	v_mov_b32_e32 v171, v68
	v_mov_b32_e32 v173, v70
	v_mov_b32_e32 v175, v72
	v_mov_b32_e32 v177, v74
	v_mov_b32_e32 v179, v76
	v_mov_b32_e32 v181, v78
	v_mov_b32_e32 v183, v80
	v_mov_b32_e32 v185, v82
	v_mov_b32_e32 v187, v84
	v_mov_b32_e32 v189, v86
	v_mov_b32_e32 v191, v88
	v_mov_b32_e32 v193, v90
	v_mov_b32_e32 v162, v58
	v_mov_b32_e32 v165, v62
	v_mov_b32_e32 v168, v65
	v_mov_b32_e32 v170, v67
	v_mov_b32_e32 v172, v69
	v_mov_b32_e32 v174, v71
	v_mov_b32_e32 v176, v73
	v_mov_b32_e32 v178, v75
	v_mov_b32_e32 v180, v77
	v_mov_b32_e32 v182, v79
	v_mov_b32_e32 v184, v81
	v_mov_b32_e32 v186, v83
	v_mov_b32_e32 v188, v85
	v_mov_b32_e32 v190, v87
	v_mov_b32_e32 v192, v89
	v_mov_b32_e32 v196, v91
	v_mov_b32_e32 v127, v20
	v_mov_b32_e32 v130, v23
	v_mov_b32_e32 v146, v41
	v_mov_b32_e32 v126, v21
	v_mov_b32_e32 v129, v22
	v_mov_b32_e32 v132, v26
	v_mov_b32_e32 v134, v30
	v_mov_b32_e32 v136, v31
	v_mov_b32_e32 v138, v34
	v_mov_b32_e32 v140, v35
	v_mov_b32_e32 v142, v37
	v_mov_b32_e32 v144, v39
	v_mov_b32_e32 v147, v44
	v_mov_b32_e32 v149, v46
	v_mov_b32_e32 v151, v48
	v_mov_b32_e32 v153, v50
	v_mov_b32_e32 v155, v52
	v_mov_b32_e32 v157, v54
	v_mov_b32_e32 v159, v56
	v_mov_b32_e32 v164, v61
	v_mov_b32_e32 v128, v24
	v_mov_b32_e32 v131, v25
	v_mov_b32_e32 v133, v27
	v_mov_b32_e32 v135, v29
	v_mov_b32_e32 v137, v32
	v_mov_b32_e32 v139, v33
	v_mov_b32_e32 v141, v36
	v_mov_b32_e32 v143, v38
	v_mov_b32_e32 v145, v43
	v_mov_b32_e32 v148, v45
	v_mov_b32_e32 v150, v47
	v_mov_b32_e32 v152, v49
	v_mov_b32_e32 v154, v51
	v_mov_b32_e32 v156, v53
	v_mov_b32_e32 v158, v55
	v_mov_b32_e32 v161, v59
	v_mov_b32_e32 v167, v64
	v_mov_b32_e32 v197, v40
	v_mov_b32_e32 v198, v42
	v_mov_b32_e32 v200, v95
	v_mov_b32_e32 v201, v94
	v_mov_b32_e32 v202, v28
	v_mov_b32_e32 v203, v3
	v_mov_b32_e32 v204, v212
	v_mov_b32_e32 v205, v213
	v_mov_b32_e32 v206, v214
	v_mov_b32_e32 v207, v215
	v_mov_b32_e32 v208, v92
	v_mov_b32_e32 v209, v93
	v_mov_b32_e32 v210, v96
	v_mov_b32_e32 v211, v97
	v_readlane_b32 s81, v252, 1
	v_readlane_b32 s82, v252, 2
	v_readlane_b32 s83, v252, 3
	v_readlane_b32 s88, v252, 8
	v_readlane_b32 s89, v252, 9
	v_readlane_b32 s92, v252, 12
	v_readlane_b32 s93, v252, 13
	v_readlane_b32 s94, v252, 14
	v_readlane_b32 s95, v252, 15
	s_branch .Lpr_476

; __device__ __forceinline__ float fast_sigmoid(float x) { return __builtin_amdgcn_rcpf(1.0f + __builtin_amdgcn_exp2f(-1.4426950408889634f * x)); }
; __global__ void __launch_bounds__(NTHR, 2) mk_fwd(Args args) {
;     ...
;                     float Wc = 1.f;
; #pragma unroll
;                     for (int t = 0; t < 16; ++t) {
;                         const float cr = xr_[t + 1], ck = xk_[t + 1], cv = xv_[t + 1], wl = xwl_[t] + c_w0, al = xal_[t] + c_a0;
;                         const float pr_r = xr_[t], pr_k = xk_[t], pr_v = xv_[t];
;                         const float r = cr + (pr_r - cr) * mu_r, k = ck + (pr_k - ck) * mu_k, v = cv + (pr_v - cv) * mu_v;
;                         const float dec = fast_decay(wl), a = fast_sigmoid(al);
;                         float kk = k * c_kk; const float ss = wave_sum_dpp(kk * kk); kk = kk * __builtin_amdgcn_rsqf(fmaxf(ss, 1e-24f));
;                         const float k2 = k * (1.0f + (a - 1.0f) * c_ka), bb = kk * a;
;                         const float Wprev = Wc; Wc = Wc * dec; const float iw = __builtin_amdgcn_rcpf(Wc);
;                         At[t] = -kk * Wprev; Rt[t] = r * Wc; Bt[t] = bb * iw; Kt[t] = k2 * iw; Vt[t] = v;
;                     }
.Lpr_478:
	s_ashr_i32 s1, s34, 8
	s_and_b32 s0, s34, 15
	s_and_b32 s1, s1, -16
	s_or_b32 s0, s1, s0
	s_bfe_u32 s35, s34, 0x80004
	s_sub_i32 s99, s35, 4
	s_ashr_i32 s1, s0, 31
	s_lshl_b64 s[0:1], s[0:1], 22
	s_lshl_b32 s34, s35, 14
	s_add_u32 s0, s29, s0
	s_addc_u32 s1, s31, s1
	v_lshlrev_b32_e32 v231, 16, v38
	v_lshlrev_b32_e32 v38, 16, v58
	s_mov_b32 s88, s100
	v_add_f32_e32 v38, v95, v38
	v_lshlrev_b32_e32 v225, 16, v47
	s_mov_b32 s89, 0
	s_sub_i32 s100, s100, 14336
	s_cmp_lt_i32 s100, 0
	s_cbranch_scc0 .Lpr_s100ok
	s_add_i32 s100, s100, 71680
.Lpr_s100ok:
	v_mul_f32_e64 v47, |v38|, s79
	s_cmp_eq_u32 s35, 0
	v_exp_f32_e32 v47, v47
	v_lshlrev_b32_e32 v234, 16, v24
	s_cselect_b64 s[0:1], -1, 0
	v_lshlrev_b32_e32 v236, 16, v25
	v_lshlrev_b32_e32 v228, 16, v39
	v_lshlrev_b32_e32 v224, 16, v46
	v_lshlrev_b32_e32 v39, 16, v57
	v_cndmask_b32_e64 v46, v234, 0, s[0:1]
	v_lshlrev_b32_e32 v222, 16, v48
	v_add_f32_e32 v48, v94, v39
	v_sub_f32_e32 v39, v46, v236
	v_lshlrev_b32_e32 v218, 16, v52
	v_fma_f32 v52, v40, v39, v236
	v_add_f32_e32 v39, 1.0, v47
	v_lshlrev_b32_e32 v235, 16, v21
	v_log_f32_e32 v46, v39
	v_lshlrev_b32_e32 v237, 16, v22
	v_lshlrev_b32_e32 v226, 16, v44
	v_cndmask_b32_e64 v44, v235, 0, s[0:1]
	v_sub_f32_e32 v39, v44, v237
	v_mul_f32_e32 v44, 0xbfb8aa3b, v48
	v_max_f32_e64 v38, -v38, 0
	v_exp_f32_e32 v44, v44
	v_fmac_f32_e32 v38, 0x3f317218, v46
	v_fma_f32 v39, v42, v39, v237
	v_add_f32_e32 v38, 0.5, v38
	v_mul_f32_e32 v38, 0xbfb8aa3b, v38
	v_mul_f32_e32 v47, v28, v39
	v_exp_f32_e32 v46, v38
	v_add_f32_e32 v38, 1.0, v44
	v_mul_f32_e32 v44, v47, v47
	v_mov_b32_e32 v48, 0
	v_lshlrev_b32_e32 v4, 16, v20
	v_mov_b32_dpp v44, v44 quad_perm:[1,0,3,2] row_mask:0xf bank_mask:0xf bound_ctrl:1
	v_fmac_f32_e32 v44, v47, v47
	v_cndmask_b32_e64 v4, v4, 0, s[0:1]
	v_rcp_f32_e32 v38, v38
	v_add_f32_dpp v44, v44, v44 quad_perm:[2,3,0,1] row_mask:0xf bank_mask:0xf bound_ctrl:1
	v_lshlrev_b32_e32 v227, 16, v45
	v_lshlrev_b32_e32 v45, 16, v62
	v_add_f32_dpp v44, v44, v44 row_half_mirror row_mask:0xf bank_mask:0xf bound_ctrl:1
	v_lshlrev_b32_e32 v5, 16, v23
	v_and_b32_e32 v23, 0xffff0000, v214
	v_add_f32_dpp v44, v44, v44 row_mirror row_mask:0xf bank_mask:0xf bound_ctrl:1
	v_lshlrev_b32_e32 v22, 16, v214
	v_lshlrev_b32_e32 v223, 16, v49
	v_mov_b32_dpp v48, v44 row_bcast:15 row_mask:0xa bank_mask:0xf
	v_add_f32_e32 v44, v44, v48
	v_mov_b32_e32 v48, 0
	v_lshlrev_b32_e32 v49, 16, v60
	v_lshlrev_b32_e32 v239, 16, v26
	v_mov_b32_dpp v48, v44 row_bcast:31 row_mask:0xc bank_mask:0xf
	v_add_f32_e32 v44, v44, v48
	v_and_b32_e32 v21, 0xffff0000, v215
	v_readlane_b32 s0, v44, 63
	v_lshlrev_b32_e32 v20, 16, v215
	v_lshlrev_b32_e32 v219, 16, v53
	v_max_f32_e64 v44, s0, s0
	v_max_f32_e32 v44, 0x179abe15, v44
	v_rsq_f32_e32 v48, v44
	v_mul_f32_e32 v44, 0xbfb8aa3b, v46
	v_exp_f32_e32 v44, v44
	v_mov_b32_e32 v53, 0
	v_mul_f32_e32 v46, v47, v48
	v_add_f32_e32 v47, -1.0, v38
	v_fma_f32 v47, v3, v47, 1.0
	v_xor_b32_e32 v214, 0x80000000, v46
	v_pk_mul_f32 v[38:39], v[38:39], v[46:47]
	v_add_f32_e32 v46, v95, v45
	v_mul_f32_e64 v45, |v46|, s79
	v_exp_f32_e32 v47, v45
	v_rcp_f32_e32 v48, v44
	v_max_f32_e64 v46, -v46, 0
	v_mul_f32_e32 v215, v52, v44
	v_add_f32_e32 v47, 1.0, v47
	v_pk_mul_f32 v[38:39], v[38:39], v[48:49] op_sel_hi:[1,0]
	v_add_f32_e32 v48, v94, v49
	v_log_f32_e32 v49, v47
	v_mul_f32_e32 v48, 0xbfb8aa3b, v48
	v_exp_f32_e32 v48, v48
	v_sub_f32_e32 v47, v237, v239
	v_fmac_f32_e32 v46, 0x3f317218, v49
	v_add_f32_e32 v46, 0.5, v46
	v_fma_f32 v47, v42, v47, v239
	v_mul_f32_e32 v46, 0xbfb8aa3b, v46
	v_exp_f32_e32 v49, v46
	v_add_f32_e32 v46, 1.0, v48
	v_mul_f32_e32 v48, v28, v47
	v_mul_f32_e32 v52, v48, v48
	v_rcp_f32_e32 v46, v46
	v_mul_f32_e32 v49, 0xbfb8aa3b, v49
	v_mov_b32_dpp v52, v52 quad_perm:[1,0,3,2] row_mask:0xf bank_mask:0xf bound_ctrl:1
	v_fmac_f32_e32 v52, v48, v48
	v_lshlrev_b32_e32 v220, 16, v50
	v_lshlrev_b32_e32 v50, 16, v65
	v_add_f32_dpp v52, v52, v52 quad_perm:[2,3,0,1] row_mask:0xf bank_mask:0xf bound_ctrl:1
	v_lshlrev_b32_e32 v241, 16, v30
	v_lshlrev_b32_e32 v242, 16, v32
	v_add_f32_dpp v52, v52, v52 row_half_mirror row_mask:0xf bank_mask:0xf bound_ctrl:1
	v_lshlrev_b32_e32 v244, 16, v33
	v_lshlrev_b32_e32 v221, 16, v51
	v_add_f32_dpp v52, v52, v52 row_mirror row_mask:0xf bank_mask:0xf bound_ctrl:1
	v_and_b32_e32 v33, 0xffff0000, v96
	v_lshlrev_b32_e32 v32, 16, v96
	v_mov_b32_dpp v53, v52 row_bcast:15 row_mask:0xa bank_mask:0xf
	v_add_f32_e32 v52, v52, v53
	v_mov_b32_e32 v53, 0
	v_lshlrev_b32_e32 v96, 16, v54
	v_lshlrev_b32_e32 v51, 16, v63
	v_mov_b32_dpp v53, v52 row_bcast:31 row_mask:0xc bank_mask:0xf
	v_add_f32_e32 v52, v52, v53
	v_exp_f32_e32 v53, v49
	v_readlane_b32 s0, v52, 63
	v_add_f32_e32 v49, -1.0, v46
	v_fma_f32 v49, v3, v49, 1.0
	v_max_f32_e64 v52, s0, s0
	v_max_f32_e32 v52, 0x179abe15, v52
	v_rsq_f32_e32 v52, v52
	v_sub_f32_e32 v54, v239, v241
	v_lshlrev_b32_e32 v243, 16, v31
	v_and_b32_e32 v31, 0xffff0000, v97
	v_mul_f32_e32 v48, v48, v52
	v_xor_b32_e32 v52, 0x80000000, v48
	v_pk_mul_f32 v[46:47], v[46:47], v[48:49]
	v_add_f32_e32 v48, v95, v50
	v_mul_f32_e64 v49, |v48|, s79
	v_exp_f32_e32 v50, v49
	v_lshlrev_b32_e32 v30, 16, v97
	v_lshlrev_b32_e32 v97, 16, v55
	v_add_f32_e32 v51, v94, v51
	v_add_f32_e32 v50, 1.0, v50
	v_log_f32_e32 v50, v50
	v_fma_f32 v55, v42, v54, v241
	v_max_f32_e64 v48, -v48, 0
	v_lshlrev_b32_e32 v238, 16, v27
	v_fmac_f32_e32 v48, 0x3f317218, v50
	v_mul_f32_e32 v50, 0xbfb8aa3b, v51
	v_mul_f32_e32 v51, v28, v55
	v_mul_f32_e32 v54, v51, v51
	v_lshlrev_b32_e32 v26, 16, v212
	v_and_b32_e32 v27, 0xffff0000, v212
	v_mov_b32_dpp v54, v54 quad_perm:[1,0,3,2] row_mask:0xf bank_mask:0xf bound_ctrl:1
; __device__ __forceinline__ float fast_sigmoid(float x) { return __builtin_amdgcn_rcpf(1.0f + __builtin_amdgcn_exp2f(-1.4426950408889634f * x)); }
; __global__ void __launch_bounds__(NTHR, 2) mk_fwd(Args args) {
;     ...
;                     for (int t = 0; t < 16; ++t) {
;                         const float cr = xr_[t + 1], ck = xk_[t + 1], cv = xv_[t + 1], wl = xwl_[t] + c_w0, al = xal_[t] + c_a0;
;                         const float pr_r = xr_[t], pr_k = xk_[t], pr_v = xv_[t];
;                         const float r = cr + (pr_r - cr) * mu_r, k = ck + (pr_k - ck) * mu_k, v = cv + (pr_v - cv) * mu_v;
;                         const float dec = fast_decay(wl), a = fast_sigmoid(al);
;                         float kk = k * c_kk; const float ss = wave_sum_dpp(kk * kk); kk = kk * __builtin_amdgcn_rsqf(fmaxf(ss, 1e-24f));
;                         const float k2 = k * (1.0f + (a - 1.0f) * c_ka), bb = kk * a;
;                         const float Wprev = Wc; Wc = Wc * dec; const float iw = __builtin_amdgcn_rcpf(Wc);
;                         At[t] = -kk * Wprev; Rt[t] = r * Wc; Bt[t] = bb * iw; Kt[t] = k2 * iw; Vt[t] = v;
;                     }
	v_fmac_f32_e32 v54, v51, v51
	v_lshlrev_b32_e32 v212, 16, v56
	v_mov_b32_e32 v56, 0
	v_add_f32_dpp v54, v54, v54 quad_perm:[2,3,0,1] row_mask:0xf bank_mask:0xf bound_ctrl:1
	v_exp_f32_e32 v50, v50
	v_add_f32_e32 v48, 0.5, v48
	v_add_f32_dpp v54, v54, v54 row_half_mirror row_mask:0xf bank_mask:0xf bound_ctrl:1
	v_mul_f32_e32 v48, 0xbfb8aa3b, v48
	v_exp_f32_e32 v48, v48
	v_add_f32_dpp v54, v54, v54 row_mirror row_mask:0xf bank_mask:0xf bound_ctrl:1
	v_add_f32_e32 v50, 1.0, v50
	v_mul_f32_e32 v53, v44, v53
	v_mov_b32_dpp v56, v54 row_bcast:15 row_mask:0xa bank_mask:0xf
	v_add_f32_e32 v54, v54, v56
	v_mov_b32_e32 v56, 0
	v_rcp_f32_e32 v58, v53
	v_sub_f32_e32 v45, v236, v238
	v_mov_b32_dpp v56, v54 row_bcast:31 row_mask:0xc bank_mask:0xf
	v_add_f32_e32 v54, v54, v56
	v_mul_f32_e32 v48, 0xbfb8aa3b, v48
	v_readlane_b32 s0, v54, 63
	v_lshlrev_b32_e32 v229, 16, v43
	v_and_b32_e32 v25, 0xffff0000, v213
	v_max_f32_e64 v54, s0, s0
	v_max_f32_e32 v54, 0x179abe15, v54
	v_rsq_f32_e32 v56, v54
	v_rcp_f32_e32 v54, v50
	v_lshlrev_b32_e32 v24, 16, v213
	v_lshlrev_b32_e32 v213, 16, v59
	v_lshlrev_b32_e32 v43, 16, v64
	v_lshlrev_b32_e32 v59, 16, v67
	v_fma_f32 v45, v40, v45, v238
	v_exp_f32_e32 v64, v48
	v_add_f32_e32 v48, -1.0, v54
	v_mul_f32_e32 v56, v51, v56
	v_fma_f32 v57, v3, v48, 1.0
	v_pk_mul_f32 v[50:51], v[44:45], v[52:53]
	v_add_f32_e32 v52, v95, v59
	v_pk_mul_f32 v[44:45], v[46:47], v[58:59] op_sel_hi:[1,0]
	v_pk_mul_f32 v[46:47], v[54:55], v[56:57]
	v_mul_f32_e64 v54, |v52|, s79
	v_exp_f32_e32 v54, v54
	v_lshlrev_b32_e32 v240, 16, v29
	v_xor_b32_e32 v48, 0x80000000, v56
	v_sub_f32_e32 v56, v240, v242
	v_add_f32_e32 v54, 1.0, v54
	v_log_f32_e32 v54, v54
	v_lshlrev_b32_e32 v60, 16, v66
	v_fma_f32 v57, v40, v56, v242
	v_sub_f32_e32 v56, v241, v243
	v_add_f32_e32 v55, v94, v60
	v_fma_f32 v59, v42, v56, v243
	v_max_f32_e64 v52, -v52, 0
	v_fmac_f32_e32 v52, 0x3f317218, v54
	v_mul_f32_e32 v54, 0xbfb8aa3b, v55
	v_mul_f32_e32 v55, v28, v59
	v_mul_f32_e32 v56, v55, v55
	v_exp_f32_e32 v54, v54
	v_mov_b32_e32 v58, 0
	v_mov_b32_dpp v56, v56 quad_perm:[1,0,3,2] row_mask:0xf bank_mask:0xf bound_ctrl:1
	v_fmac_f32_e32 v56, v55, v55
	v_add_f32_e32 v52, 0.5, v52
	v_mul_f32_e32 v52, 0xbfb8aa3b, v52
	v_add_f32_dpp v56, v56, v56 quad_perm:[2,3,0,1] row_mask:0xf bank_mask:0xf bound_ctrl:1
	v_exp_f32_e32 v52, v52
	v_add_f32_e32 v54, 1.0, v54
	v_add_f32_dpp v56, v56, v56 row_half_mirror row_mask:0xf bank_mask:0xf bound_ctrl:1
	v_lshlrev_b32_e32 v249, 16, v72
	v_mul_f32_e32 v52, 0xbfb8aa3b, v52
	v_add_f32_dpp v56, v56, v56 row_mirror row_mask:0xf bank_mask:0xf bound_ctrl:1
	v_exp_f32_e32 v72, v52
	v_mul_f32_e32 v65, v53, v64
	v_mov_b32_dpp v58, v56 row_bcast:15 row_mask:0xa bank_mask:0xf
	v_add_f32_e32 v56, v56, v58
	v_mov_b32_e32 v58, 0
	v_lshlrev_b32_e32 v29, 16, v41
	v_lshlrev_b32_e32 v41, 16, v61
	v_mov_b32_dpp v58, v56 row_bcast:31 row_mask:0xc bank_mask:0xf
	v_add_f32_e32 v56, v56, v58
	v_rcp_f32_e32 v58, v54
	v_readlane_b32 s0, v56, 63
	v_lshlrev_b32_e32 v69, 16, v69
	v_sub_f32_e32 v49, v238, v240
	v_max_f32_e64 v56, s0, s0
	v_add_f32_e32 v52, -1.0, v58
	v_max_f32_e32 v56, 0x179abe15, v56
	v_fma_f32 v61, v3, v52, 1.0
	v_rcp_f32_e32 v52, v65
	v_rsq_f32_e32 v56, v56
	v_fma_f32 v49, v40, v49, v240
	v_mov_b32_e32 v64, v53
	v_pk_mul_f32 v[46:47], v[46:47], v[52:53] op_sel_hi:[1,0]
	v_add_f32_e32 v52, v95, v69
	v_mul_f32_e32 v60, v55, v56
	v_mul_f32_e64 v53, |v52|, s79
	v_pk_mul_f32 v[54:55], v[64:65], v[48:49]
	v_pk_mul_f32 v[48:49], v[58:59], v[60:61]
	v_exp_f32_e32 v58, v53
	v_lshlrev_b32_e32 v245, 16, v34
	v_lshlrev_b32_e32 v68, 16, v68
	v_sub_f32_e32 v59, v243, v245
	v_add_f32_e32 v58, 1.0, v58
	v_log_f32_e32 v58, v58
	v_xor_b32_e32 v56, 0x80000000, v60
	v_add_f32_e32 v60, v94, v68
	v_fma_f32 v59, v42, v59, v245
	v_max_f32_e64 v52, -v52, 0
	v_fmac_f32_e32 v52, 0x3f317218, v58
	v_mul_f32_e32 v58, 0xbfb8aa3b, v60
	v_mul_f32_e32 v60, v28, v59
	v_mul_f32_e32 v61, v60, v60
	v_mov_b32_e32 v64, 0
	v_exp_f32_e32 v58, v58
	v_mov_b32_dpp v61, v61 quad_perm:[1,0,3,2] row_mask:0xf bank_mask:0xf bound_ctrl:1
	v_fmac_f32_e32 v61, v60, v60
	v_add_f32_e32 v52, 0.5, v52
	v_mul_f32_e32 v52, 0xbfb8aa3b, v52
	v_add_f32_dpp v61, v61, v61 quad_perm:[2,3,0,1] row_mask:0xf bank_mask:0xf bound_ctrl:1
	v_exp_f32_e32 v52, v52
	v_add_f32_e32 v58, 1.0, v58
	v_add_f32_dpp v61, v61, v61 row_half_mirror row_mask:0xf bank_mask:0xf bound_ctrl:1
	v_rcp_f32_e32 v58, v58
	v_mul_f32_e32 v52, 0xbfb8aa3b, v52
	v_add_f32_dpp v61, v61, v61 row_mirror row_mask:0xf bank_mask:0xf bound_ctrl:1
	v_lshlrev_b32_e32 v62, 16, v74
	v_lshlrev_b32_e32 v74, 16, v80
	v_mov_b32_dpp v64, v61 row_bcast:15 row_mask:0xa bank_mask:0xf
	v_add_f32_e32 v61, v61, v64
	v_mov_b32_e32 v64, 0
	v_exp_f32_e32 v80, v52
	v_add_f32_e32 v52, -1.0, v58
	v_mov_b32_dpp v64, v61 row_bcast:31 row_mask:0xc bank_mask:0xf
	v_add_f32_e32 v61, v61, v64
	v_lshlrev_b32_e32 v246, 16, v71
	v_readlane_b32 s0, v61, 63
	v_lshlrev_b32_e32 v248, 16, v73
	v_fma_f32 v69, v3, v52, 1.0
	v_max_f32_e64 v61, s0, s0
	v_max_f32_e32 v61, 0x179abe15, v61
	v_rsq_f32_e32 v61, v61
	v_mul_f32_e32 v73, v65, v72
	v_mov_b32_e32 v72, v65
	v_rcp_f32_e32 v64, v73
	v_mul_f32_e32 v68, v60, v61
	v_pk_mul_f32 v[60:61], v[72:73], v[56:57]
	v_pk_mul_f32 v[56:57], v[58:59], v[68:69]
	v_add_f32_e32 v58, v95, v246
	v_mul_f32_e64 v59, |v58|, s79
	v_exp_f32_e32 v59, v59
	v_lshlrev_b32_e32 v233, 16, v36
	v_pk_mul_f32 v[48:49], v[48:49], v[64:65] op_sel_hi:[1,0]
	v_sub_f32_e32 v65, v244, v233
	v_add_f32_e32 v59, 1.0, v59
	v_lshlrev_b32_e32 v247, 16, v70
	v_fma_f32 v69, v40, v65, v233
	v_log_f32_e32 v65, v59
	v_add_f32_e32 v64, v94, v247
	v_mul_f32_e32 v64, 0xbfb8aa3b, v64
	v_max_f32_e64 v58, -v58, 0
; __device__ __forceinline__ float fast_sigmoid(float x) { return __builtin_amdgcn_rcpf(1.0f + __builtin_amdgcn_exp2f(-1.4426950408889634f * x)); }
; __global__ void __launch_bounds__(NTHR, 2) mk_fwd(Args args) {
;     ...
;                     for (int t = 0; t < 16; ++t) {
;                         const float cr = xr_[t + 1], ck = xk_[t + 1], cv = xv_[t + 1], wl = xwl_[t] + c_w0, al = xal_[t] + c_a0;
;                         const float pr_r = xr_[t], pr_k = xk_[t], pr_v = xv_[t];
;                         const float r = cr + (pr_r - cr) * mu_r, k = ck + (pr_k - ck) * mu_k, v = cv + (pr_v - cv) * mu_v;
;                         const float dec = fast_decay(wl), a = fast_sigmoid(al);
;                         float kk = k * c_kk; const float ss = wave_sum_dpp(kk * kk); kk = kk * __builtin_amdgcn_rsqf(fmaxf(ss, 1e-24f));
;                         const float k2 = k * (1.0f + (a - 1.0f) * c_ka), bb = kk * a;
;                         const float Wprev = Wc; Wc = Wc * dec; const float iw = __builtin_amdgcn_rcpf(Wc);
;                         At[t] = -kk * Wprev; Rt[t] = r * Wc; Bt[t] = bb * iw; Kt[t] = k2 * iw; Vt[t] = v;
;                     }
	v_exp_f32_e32 v64, v64
	v_lshlrev_b32_e32 v232, 16, v35
	v_fmac_f32_e32 v58, 0x3f317218, v65
	v_sub_f32_e32 v59, v245, v232
	v_add_f32_e32 v58, 0.5, v58
	v_fma_f32 v59, v42, v59, v232
	v_mul_f32_e32 v58, 0xbfb8aa3b, v58
	v_exp_f32_e32 v65, v58
	v_add_f32_e32 v58, 1.0, v64
	v_mul_f32_e32 v64, v28, v59
	v_xor_b32_e32 v52, 0x80000000, v68
	v_mul_f32_e32 v68, v64, v64
	v_mov_b32_e32 v72, 0
	v_lshlrev_b32_e32 v63, 16, v75
	v_mov_b32_dpp v68, v68 quad_perm:[1,0,3,2] row_mask:0xf bank_mask:0xf bound_ctrl:1
	v_fmac_f32_e32 v68, v64, v64
	v_lshlrev_b32_e32 v75, 16, v81
	v_rcp_f32_e32 v58, v58
	v_add_f32_dpp v68, v68, v68 quad_perm:[2,3,0,1] row_mask:0xf bank_mask:0xf bound_ctrl:1
	v_mul_f32_e32 v81, v73, v80
	v_sub_f32_e32 v53, v242, v244
	v_add_f32_dpp v68, v68, v68 row_half_mirror row_mask:0xf bank_mask:0xf bound_ctrl:1
	v_lshlrev_b32_e32 v66, 16, v76
	v_fma_f32 v53, v40, v53, v244
	v_add_f32_dpp v68, v68, v68 row_mirror row_mask:0xf bank_mask:0xf bound_ctrl:1
	v_mul_f32_e32 v65, 0xbfb8aa3b, v65
	v_mov_b32_e32 v80, v73
	v_mov_b32_dpp v72, v68 row_bcast:15 row_mask:0xa bank_mask:0xf
	v_add_f32_e32 v68, v68, v72
	v_mov_b32_e32 v72, 0
	v_and_b32_e32 v35, 0xffff0000, v93
	v_lshlrev_b32_e32 v34, 16, v93
	v_mov_b32_dpp v72, v68 row_bcast:31 row_mask:0xc bank_mask:0xf
	v_add_f32_e32 v68, v68, v72
	v_rcp_f32_e32 v72, v81
	v_readlane_b32 s0, v68, 63
	v_lshlrev_b32_e32 v67, 16, v77
	v_lshlrev_b32_e32 v93, 16, v88
	v_max_f32_e64 v68, s0, s0
	v_max_f32_e32 v68, 0x179abe15, v68
	v_rsq_f32_e32 v68, v68
	v_exp_f32_e32 v88, v65
	v_lshlrev_b32_e32 v230, 16, v37
	v_lshlrev_b32_e32 v70, 16, v78
	v_mul_f32_e32 v76, v64, v68
	v_add_f32_e32 v64, -1.0, v58
	v_fma_f32 v77, v3, v64, 1.0
	v_pk_mul_f32 v[64:65], v[80:81], v[52:53]
	v_pk_mul_f32 v[52:53], v[56:57], v[72:73] op_sel_hi:[1,0]
	v_add_f32_e32 v72, v95, v248
	v_pk_mul_f32 v[56:57], v[58:59], v[76:77]
	v_mul_f32_e64 v58, |v72|, s79
	v_exp_f32_e32 v58, v58
	v_sub_f32_e32 v59, v233, v231
	v_fma_f32 v73, v40, v59, v231
	v_sub_f32_e32 v59, v232, v230
	v_add_f32_e32 v58, 1.0, v58
	v_log_f32_e32 v80, v58
	v_fma_f32 v77, v42, v59, v230
	v_pk_add_f32 v[58:59], v[26:27], v[24:25] neg_lo:[0,1] neg_hi:[0,1]
	v_max_f32_e64 v27, -v72, 0
	v_xor_b32_e32 v68, 0x80000000, v76
	v_add_f32_e32 v76, v94, v249
	v_fmac_f32_e32 v27, 0x3f317218, v80
	v_mul_f32_e32 v80, v28, v77
	v_mul_f32_e32 v72, 0xbfb8aa3b, v76
	v_mul_f32_e32 v76, v80, v80
	v_lshlrev_b32_e32 v78, 16, v82
	v_mov_b32_e32 v82, 0
	v_mov_b32_dpp v76, v76 quad_perm:[1,0,3,2] row_mask:0xf bank_mask:0xf bound_ctrl:1
	v_fmac_f32_e32 v76, v80, v80
	v_lshlrev_b32_e32 v36, 16, v92
	v_and_b32_e32 v37, 0xffff0000, v92
	v_add_f32_dpp v76, v76, v76 quad_perm:[2,3,0,1] row_mask:0xf bank_mask:0xf bound_ctrl:1
	v_lshlrev_b32_e32 v92, 16, v89
	v_mul_f32_e32 v89, v81, v88
	v_add_f32_dpp v76, v76, v76 row_half_mirror row_mask:0xf bank_mask:0xf bound_ctrl:1
	v_exp_f32_e32 v72, v72
	v_add_f32_e32 v63, v95, v63
	v_add_f32_dpp v76, v76, v76 row_mirror row_mask:0xf bank_mask:0xf bound_ctrl:1
	v_lshlrev_b32_e32 v71, 16, v79
	v_add_f32_e32 v72, 1.0, v72
	v_mov_b32_dpp v82, v76 row_bcast:15 row_mask:0xa bank_mask:0xf
	v_add_f32_e32 v76, v76, v82
	v_mov_b32_e32 v82, 0
	v_lshlrev_b32_e32 v79, 16, v83
	v_add_f32_e32 v27, 0.5, v27
	v_mov_b32_dpp v82, v76 row_bcast:31 row_mask:0xc bank_mask:0xf
	v_add_f32_e32 v76, v76, v82
	v_mul_f32_e32 v27, 0xbfb8aa3b, v27
	v_readlane_b32 s0, v76, 63
	v_mov_b32_e32 v88, v81
	v_exp_f32_e32 v27, v27
	v_max_f32_e64 v76, s0, s0
	v_max_f32_e32 v76, 0x179abe15, v76
	v_rsq_f32_e32 v82, v76
	v_rcp_f32_e32 v76, v72
	v_pk_mul_f32 v[68:69], v[88:89], v[68:69]
	v_mov_b32_e32 v88, 0
	v_mul_f32_e32 v82, v80, v82
	v_rcp_f32_e32 v80, v89
	v_add_f32_e32 v72, -1.0, v76
	v_fma_f32 v83, v3, v72, 1.0
	v_xor_b32_e32 v72, 0x80000000, v82
	v_pk_mul_f32 v[56:57], v[56:57], v[80:81] op_sel_hi:[1,0]
	v_mul_f32_e64 v80, |v63|, s79
	v_exp_f32_e32 v80, v80
	v_pk_mul_f32 v[76:77], v[76:77], v[82:83]
	v_sub_f32_e32 v82, v230, v228
	v_fma_f32 v83, v42, v82, v228
	v_add_f32_e32 v80, 1.0, v80
	v_log_f32_e32 v80, v80
	v_max_f32_e64 v63, -v63, 0
	v_add_f32_e32 v62, v94, v62
	v_mul_f32_e32 v62, 0xbfb8aa3b, v62
	v_fmac_f32_e32 v63, 0x3f317218, v80
	v_mul_f32_e32 v80, v28, v83
	v_mul_f32_e32 v82, v80, v80
	v_exp_f32_e32 v62, v62
	v_mul_f32_e32 v27, 0xbfb8aa3b, v27
	v_mov_b32_dpp v82, v82 quad_perm:[1,0,3,2] row_mask:0xf bank_mask:0xf bound_ctrl:1
	v_fmac_f32_e32 v82, v80, v80
	v_exp_f32_e32 v27, v27
	v_add_f32_e32 v63, 0.5, v63
	v_add_f32_dpp v82, v82, v82 quad_perm:[2,3,0,1] row_mask:0xf bank_mask:0xf bound_ctrl:1
	v_mul_f32_e32 v63, 0xbfb8aa3b, v63
	v_exp_f32_e32 v63, v63
	v_add_f32_dpp v82, v82, v82 row_half_mirror row_mask:0xf bank_mask:0xf bound_ctrl:1
	v_add_f32_e32 v62, 1.0, v62
	v_sub_f32_e32 v81, v231, v229
	v_add_f32_dpp v82, v82, v82 row_mirror row_mask:0xf bank_mask:0xf bound_ctrl:1
	v_mul_f32_e32 v231, v89, v27
	v_add_f32_e32 v27, v95, v67
	v_mov_b32_dpp v88, v82 row_bcast:15 row_mask:0xa bank_mask:0xf
	v_add_f32_e32 v82, v82, v88
	v_mov_b32_e32 v88, 0
	v_mul_f32_e64 v67, |v27|, s79
	v_exp_f32_e32 v67, v67
	v_mov_b32_dpp v88, v82 row_bcast:31 row_mask:0xc bank_mask:0xf
	v_add_f32_e32 v82, v82, v88
	v_lshlrev_b32_e32 v217, 16, v91
	v_readlane_b32 s0, v82, 63
	v_add_f32_e32 v67, 1.0, v67
	v_log_f32_e32 v67, v67
	v_max_f32_e64 v82, s0, s0
	v_max_f32_e32 v82, 0x179abe15, v82
	v_rsq_f32_e32 v88, v82
	v_rcp_f32_e32 v82, v62
	v_mul_f32_e32 v62, 0xbfb8aa3b, v63
	v_exp_f32_e32 v232, v62
	v_lshlrev_b32_e32 v216, 16, v90
	v_add_f32_e32 v62, -1.0, v82
	v_fma_f32 v91, v3, v62, 1.0
	v_rcp_f32_e32 v62, v231
	v_mul_f32_e32 v90, v80, v88
	v_mov_b32_e32 v230, v89
	v_pk_mul_f32 v[82:83], v[82:83], v[90:91]
; __device__ __forceinline__ float fast_sigmoid(float x) { return __builtin_amdgcn_rcpf(1.0f + __builtin_amdgcn_exp2f(-1.4426950408889634f * x)); }
; __global__ void __launch_bounds__(NTHR, 2) mk_fwd(Args args) {
;     ...
;                     for (int t = 0; t < 16; ++t) {
;                         const float cr = xr_[t + 1], ck = xk_[t + 1], cv = xv_[t + 1], wl = xwl_[t] + c_w0, al = xal_[t] + c_a0;
;                         const float pr_r = xr_[t], pr_k = xk_[t], pr_v = xv_[t];
;                         const float r = cr + (pr_r - cr) * mu_r, k = ck + (pr_k - ck) * mu_k, v = cv + (pr_v - cv) * mu_v;
;                         const float dec = fast_decay(wl), a = fast_sigmoid(al);
;                         float kk = k * c_kk; const float ss = wave_sum_dpp(kk * kk); kk = kk * __builtin_amdgcn_rsqf(fmaxf(ss, 1e-24f));
;                         const float k2 = k * (1.0f + (a - 1.0f) * c_ka), bb = kk * a;
;                         const float Wprev = Wc; Wc = Wc * dec; const float iw = __builtin_amdgcn_rcpf(Wc);
;                         At[t] = -kk * Wprev; Rt[t] = r * Wc; Bt[t] = bb * iw; Kt[t] = k2 * iw; Vt[t] = v;
;                     }
	v_pk_mul_f32 v[62:63], v[76:77], v[62:63] op_sel_hi:[1,0]
	v_sub_f32_e32 v76, v229, v227
	v_fma_f32 v89, v40, v76, v227
	v_sub_f32_e32 v76, v228, v226
	v_fma_f32 v91, v42, v76, v226
	v_max_f32_e64 v27, -v27, 0
	v_fmac_f32_e32 v27, 0x3f317218, v67
	v_mul_f32_e32 v67, v28, v91
	v_mul_f32_e32 v76, v67, v67
	v_mov_b32_e32 v77, 0
	v_add_f32_e32 v66, v94, v66
	v_mov_b32_dpp v76, v76 quad_perm:[1,0,3,2] row_mask:0xf bank_mask:0xf bound_ctrl:1
	v_fmac_f32_e32 v76, v67, v67
	v_mul_f32_e32 v66, 0xbfb8aa3b, v66
	v_exp_f32_e32 v66, v66
	v_add_f32_dpp v76, v76, v76 quad_perm:[2,3,0,1] row_mask:0xf bank_mask:0xf bound_ctrl:1
	v_fma_f32 v81, v40, v81, v229
	v_xor_b32_e32 v80, 0x80000000, v90
	v_add_f32_dpp v76, v76, v76 row_half_mirror row_mask:0xf bank_mask:0xf bound_ctrl:1
	v_add_f32_e32 v66, 1.0, v66
	v_rcp_f32_e32 v90, v66
	v_add_f32_dpp v76, v76, v76 row_mirror row_mask:0xf bank_mask:0xf bound_ctrl:1
	v_mul_f32_e32 v233, v231, v232
	v_mov_b32_e32 v232, v231
	v_mov_b32_dpp v77, v76 row_bcast:15 row_mask:0xa bank_mask:0xf
	v_add_f32_e32 v76, v76, v77
	v_mov_b32_e32 v77, 0
	v_add_f32_e32 v71, v95, v71
	v_add_f32_e32 v66, -1.0, v90
	v_mov_b32_dpp v77, v76 row_bcast:31 row_mask:0xc bank_mask:0xf
	v_add_f32_e32 v76, v76, v77
	v_fma_f32 v229, v3, v66, 1.0
	v_readlane_b32 s0, v76, 63
	v_rcp_f32_e32 v66, v233
	v_add_f32_e32 v27, 0.5, v27
	v_max_f32_e64 v76, s0, s0
	v_max_f32_e32 v76, 0x179abe15, v76
	v_rsq_f32_e32 v76, v76
	v_mul_f32_e32 v27, 0xbfb8aa3b, v27
	v_exp_f32_e32 v27, v27
	v_add_f32_e32 v70, v94, v70
	v_mul_f32_e32 v228, v67, v76
	v_pk_mul_f32 v[76:77], v[232:233], v[80:81]
	v_mul_f32_e64 v80, |v71|, s79
	v_exp_f32_e32 v80, v80
	v_sub_f32_e32 v81, v227, v225
	v_pk_mul_f32 v[66:67], v[82:83], v[66:67] op_sel_hi:[1,0]
	v_pk_mul_f32 v[82:83], v[90:91], v[228:229]
	v_add_f32_e32 v80, 1.0, v80
	v_log_f32_e32 v80, v80
	v_fma_f32 v91, v40, v81, v225
	v_sub_f32_e32 v81, v226, v224
	v_fma_f32 v227, v42, v81, v224
	v_max_f32_e64 v71, -v71, 0
	v_fmac_f32_e32 v71, 0x3f317218, v80
	v_mul_f32_e32 v80, v28, v227
	v_mul_f32_e32 v81, v80, v80
	v_mul_f32_e32 v70, 0xbfb8aa3b, v70
	v_exp_f32_e32 v70, v70
	v_mov_b32_dpp v81, v81 quad_perm:[1,0,3,2] row_mask:0xf bank_mask:0xf bound_ctrl:1
	v_fmac_f32_e32 v81, v80, v80
	v_mul_f32_e32 v27, 0xbfb8aa3b, v27
	v_exp_f32_e32 v27, v27
	v_add_f32_dpp v81, v81, v81 quad_perm:[2,3,0,1] row_mask:0xf bank_mask:0xf bound_ctrl:1
	v_add_f32_e32 v71, 0.5, v71
	v_mul_f32_e32 v71, 0xbfb8aa3b, v71
	v_add_f32_dpp v81, v81, v81 row_half_mirror row_mask:0xf bank_mask:0xf bound_ctrl:1
	v_mov_b32_e32 v90, 0
	v_exp_f32_e32 v71, v71
	v_add_f32_dpp v81, v81, v81 row_mirror row_mask:0xf bank_mask:0xf bound_ctrl:1
	v_add_f32_e32 v70, 1.0, v70
	v_rcp_f32_e32 v226, v70
	v_mov_b32_dpp v90, v81 row_bcast:15 row_mask:0xa bank_mask:0xf
	v_add_f32_e32 v81, v81, v90
	v_mov_b32_e32 v90, 0
	v_pk_mul_f32 v[72:73], v[230:231], v[72:73]
	v_mul_f32_e32 v231, v233, v27
	v_mov_b32_dpp v90, v81 row_bcast:31 row_mask:0xc bank_mask:0xf
	v_add_f32_e32 v27, v95, v75
	v_add_f32_e32 v81, v81, v90
	v_mul_f32_e64 v75, |v27|, s79
	v_readlane_b32 s0, v81, 63
	v_mul_f32_e32 v70, 0xbfb8aa3b, v71
	v_exp_f32_e32 v75, v75
	v_max_f32_e64 v81, s0, s0
	v_exp_f32_e32 v232, v70
	v_add_f32_e32 v70, -1.0, v226
	v_max_f32_e32 v81, 0x179abe15, v81
	v_fma_f32 v229, v3, v70, 1.0
	v_rcp_f32_e32 v70, v231
	v_rsq_f32_e32 v81, v81
	v_add_f32_e32 v75, 1.0, v75
	v_log_f32_e32 v75, v75
	v_pk_mul_f32 v[70:71], v[82:83], v[70:71] op_sel_hi:[1,0]
	v_sub_f32_e32 v82, v225, v223
	v_xor_b32_e32 v88, 0x80000000, v228
	v_mul_f32_e32 v228, v80, v81
	v_mov_b32_e32 v230, v233
	v_fma_f32 v225, v40, v82, v223
	v_sub_f32_e32 v82, v224, v222
	v_pk_mul_f32 v[80:81], v[230:231], v[88:89]
	v_pk_mul_f32 v[88:89], v[226:227], v[228:229]
	v_fma_f32 v227, v42, v82, v222
	v_max_f32_e64 v27, -v27, 0
	v_fmac_f32_e32 v27, 0x3f317218, v75
	v_mul_f32_e32 v75, v28, v227
	v_mul_f32_e32 v82, v75, v75
	v_add_f32_e32 v74, v94, v74
	v_mul_f32_e32 v74, 0xbfb8aa3b, v74
	v_mov_b32_dpp v82, v82 quad_perm:[1,0,3,2] row_mask:0xf bank_mask:0xf bound_ctrl:1
	v_fmac_f32_e32 v82, v75, v75
	v_exp_f32_e32 v74, v74
	v_mov_b32_e32 v83, 0
	v_add_f32_dpp v82, v82, v82 quad_perm:[2,3,0,1] row_mask:0xf bank_mask:0xf bound_ctrl:1
	v_mul_f32_e32 v233, v231, v232
	v_add_f32_e32 v74, 1.0, v74
	v_add_f32_dpp v82, v82, v82 row_half_mirror row_mask:0xf bank_mask:0xf bound_ctrl:1
	v_rcp_f32_e32 v226, v74
	v_add_f32_e32 v79, v95, v79
	v_add_f32_dpp v82, v82, v82 row_mirror row_mask:0xf bank_mask:0xf bound_ctrl:1
	v_xor_b32_e32 v90, 0x80000000, v228
	v_add_f32_e32 v74, -1.0, v226
	v_mov_b32_dpp v83, v82 row_bcast:15 row_mask:0xa bank_mask:0xf
	v_add_f32_e32 v82, v82, v83
	v_mov_b32_e32 v83, 0
	v_fma_f32 v229, v3, v74, 1.0
	v_rcp_f32_e32 v74, v233
	v_mov_b32_dpp v83, v82 row_bcast:31 row_mask:0xc bank_mask:0xf
	v_add_f32_e32 v82, v82, v83
	v_add_f32_e32 v27, 0.5, v27
	v_readlane_b32 s0, v82, 63
	v_mov_b32_e32 v232, v231
	v_mul_f32_e32 v27, 0xbfb8aa3b, v27
	v_max_f32_e64 v82, s0, s0
	v_max_f32_e32 v82, 0x179abe15, v82
	v_rsq_f32_e32 v82, v82
	v_exp_f32_e32 v27, v27
	v_add_f32_e32 v78, v94, v78
	v_mul_f32_e32 v78, 0xbfb8aa3b, v78
	v_mul_f32_e32 v228, v75, v82
	v_pk_mul_f32 v[74:75], v[88:89], v[74:75] op_sel_hi:[1,0]
	v_mul_f32_e64 v88, |v79|, s79
	v_exp_f32_e32 v88, v88
	v_sub_f32_e32 v89, v223, v221
	v_fma_f32 v223, v40, v89, v221
	v_sub_f32_e32 v89, v222, v220
	v_add_f32_e32 v88, 1.0, v88
	v_log_f32_e32 v88, v88
	v_pk_mul_f32 v[82:83], v[232:233], v[90:91]
	v_pk_mul_f32 v[90:91], v[226:227], v[228:229]
	v_fma_f32 v227, v42, v89, v220
	v_max_f32_e64 v79, -v79, 0
	v_fmac_f32_e32 v79, 0x3f317218, v88
	v_mul_f32_e32 v88, v28, v227
	v_mul_f32_e32 v89, v88, v88
; __device__ __forceinline__ float fast_sigmoid(float x) { return __builtin_amdgcn_rcpf(1.0f + __builtin_amdgcn_exp2f(-1.4426950408889634f * x)); }
; __global__ void __launch_bounds__(NTHR, 2) mk_fwd(Args args) {
;     ...
;                     for (int t = 0; t < 16; ++t) {
;                         const float cr = xr_[t + 1], ck = xk_[t + 1], cv = xv_[t + 1], wl = xwl_[t] + c_w0, al = xal_[t] + c_a0;
;                         const float pr_r = xr_[t], pr_k = xk_[t], pr_v = xv_[t];
;                         const float r = cr + (pr_r - cr) * mu_r, k = ck + (pr_k - ck) * mu_k, v = cv + (pr_v - cv) * mu_v;
;                         const float dec = fast_decay(wl), a = fast_sigmoid(al);
;                         float kk = k * c_kk; const float ss = wave_sum_dpp(kk * kk); kk = kk * __builtin_amdgcn_rsqf(fmaxf(ss, 1e-24f));
;                         const float k2 = k * (1.0f + (a - 1.0f) * c_ka), bb = kk * a;
;                         const float Wprev = Wc; Wc = Wc * dec; const float iw = __builtin_amdgcn_rcpf(Wc);
;                         At[t] = -kk * Wprev; Rt[t] = r * Wc; Bt[t] = bb * iw; Kt[t] = k2 * iw; Vt[t] = v;
;                     }
	v_exp_f32_e32 v78, v78
	v_mul_f32_e32 v27, 0xbfb8aa3b, v27
	v_mov_b32_dpp v89, v89 quad_perm:[1,0,3,2] row_mask:0xf bank_mask:0xf bound_ctrl:1
	v_fmac_f32_e32 v89, v88, v88
	v_exp_f32_e32 v27, v27
	v_add_f32_e32 v79, 0.5, v79
	v_add_f32_dpp v89, v89, v89 quad_perm:[2,3,0,1] row_mask:0xf bank_mask:0xf bound_ctrl:1
	v_mul_f32_e32 v79, 0xbfb8aa3b, v79
	v_mov_b32_e32 v222, 0
	v_add_f32_dpp v89, v89, v89 row_half_mirror row_mask:0xf bank_mask:0xf bound_ctrl:1
	v_exp_f32_e32 v79, v79
	v_add_f32_e32 v78, 1.0, v78
	v_add_f32_dpp v89, v89, v89 row_mirror row_mask:0xf bank_mask:0xf bound_ctrl:1
	v_lshlrev_b32_e32 v85, 16, v85
	v_rcp_f32_e32 v226, v78
	v_mov_b32_dpp v222, v89 row_bcast:15 row_mask:0xa bank_mask:0xf
	v_add_f32_e32 v89, v89, v222
	v_mov_b32_e32 v222, 0
	v_mul_f32_e32 v231, v233, v27
	v_add_f32_e32 v27, v95, v85
	v_mov_b32_dpp v222, v89 row_bcast:31 row_mask:0xc bank_mask:0xf
	v_add_f32_e32 v89, v89, v222
	v_mul_f32_e64 v85, |v27|, s79
	v_readlane_b32 s0, v89, 63
	v_mul_f32_e32 v78, 0xbfb8aa3b, v79
	v_exp_f32_e32 v85, v85
	v_max_f32_e64 v89, s0, s0
	v_exp_f32_e32 v232, v78
	v_add_f32_e32 v78, -1.0, v226
	v_max_f32_e32 v89, 0x179abe15, v89
	v_fma_f32 v229, v3, v78, 1.0
	v_rcp_f32_e32 v78, v231
	v_rsq_f32_e32 v89, v89
	v_add_f32_e32 v85, 1.0, v85
	v_log_f32_e32 v85, v85
	v_pk_mul_f32 v[78:79], v[90:91], v[78:79] op_sel_hi:[1,0]
	v_sub_f32_e32 v90, v221, v219
	v_xor_b32_e32 v224, 0x80000000, v228
	v_mul_f32_e32 v228, v88, v89
	v_mov_b32_e32 v230, v233
	v_fma_f32 v221, v40, v90, v219
	v_sub_f32_e32 v90, v220, v218
	v_pk_mul_f32 v[88:89], v[230:231], v[224:225]
	v_pk_mul_f32 v[224:225], v[226:227], v[228:229]
	v_fma_f32 v227, v42, v90, v218
	v_max_f32_e64 v27, -v27, 0
	v_fmac_f32_e32 v27, 0x3f317218, v85
	v_mul_f32_e32 v85, v28, v227
	v_lshlrev_b32_e32 v84, 16, v84
	v_mul_f32_e32 v90, v85, v85
	v_add_f32_e32 v84, v94, v84
	v_mul_f32_e32 v84, 0xbfb8aa3b, v84
	v_mov_b32_dpp v90, v90 quad_perm:[1,0,3,2] row_mask:0xf bank_mask:0xf bound_ctrl:1
	v_fmac_f32_e32 v90, v85, v85
	v_exp_f32_e32 v84, v84
	v_mov_b32_e32 v91, 0
	v_add_f32_dpp v90, v90, v90 quad_perm:[2,3,0,1] row_mask:0xf bank_mask:0xf bound_ctrl:1
	v_mul_f32_e32 v233, v231, v232
	v_add_f32_e32 v84, 1.0, v84
	v_add_f32_dpp v90, v90, v90 row_half_mirror row_mask:0xf bank_mask:0xf bound_ctrl:1
	v_rcp_f32_e32 v226, v84
	v_lshlrev_b32_e32 v87, 16, v87
	v_add_f32_dpp v90, v90, v90 row_mirror row_mask:0xf bank_mask:0xf bound_ctrl:1
	v_add_f32_e32 v87, v95, v87
	v_add_f32_e32 v84, -1.0, v226
	v_mov_b32_dpp v91, v90 row_bcast:15 row_mask:0xa bank_mask:0xf
	v_add_f32_e32 v90, v90, v91
	v_mov_b32_e32 v91, 0
	v_fma_f32 v229, v3, v84, 1.0
	v_rcp_f32_e32 v84, v233
	v_mov_b32_dpp v91, v90 row_bcast:31 row_mask:0xc bank_mask:0xf
	v_add_f32_e32 v90, v90, v91
	v_xor_b32_e32 v222, 0x80000000, v228
	v_readlane_b32 s0, v90, 63
	v_sub_f32_e32 v218, v218, v96
	v_mov_b32_e32 v232, v231
	v_max_f32_e64 v90, s0, s0
	v_max_f32_e32 v90, 0x179abe15, v90
	v_rsq_f32_e32 v90, v90
	v_lshlrev_b32_e32 v86, 16, v86
	v_add_f32_e32 v27, 0.5, v27
	v_add_f32_e32 v86, v94, v86
	v_mul_f32_e32 v228, v85, v90
	v_pk_mul_f32 v[84:85], v[224:225], v[84:85] op_sel_hi:[1,0]
	v_mul_f32_e64 v224, |v87|, s79
	v_exp_f32_e32 v224, v224
	v_fma_f32 v225, v42, v218, v96
	v_max_f32_e64 v87, -v87, 0
	v_mul_f32_e32 v218, v28, v225
	v_add_f32_e32 v224, 1.0, v224
	v_log_f32_e32 v224, v224
	v_pk_mul_f32 v[90:91], v[232:233], v[222:223]
	v_pk_mul_f32 v[222:223], v[226:227], v[228:229]
	v_mov_b32_e32 v226, 0
	v_fmac_f32_e32 v87, 0x3f317218, v224
	v_mul_f32_e32 v224, v218, v218
	v_mul_f32_e32 v27, 0xbfb8aa3b, v27
	v_mul_f32_e32 v86, 0xbfb8aa3b, v86
	v_mov_b32_dpp v224, v224 quad_perm:[1,0,3,2] row_mask:0xf bank_mask:0xf bound_ctrl:1
	v_fmac_f32_e32 v224, v218, v218
	v_exp_f32_e32 v27, v27
	v_exp_f32_e32 v86, v86
	v_add_f32_dpp v224, v224, v224 quad_perm:[2,3,0,1] row_mask:0xf bank_mask:0xf bound_ctrl:1
	v_add_f32_e32 v87, 0.5, v87
	v_mul_f32_e32 v87, 0xbfb8aa3b, v87
	v_add_f32_dpp v224, v224, v224 row_half_mirror row_mask:0xf bank_mask:0xf bound_ctrl:1
	v_mul_f32_e32 v27, 0xbfb8aa3b, v27
	v_exp_f32_e32 v87, v87
	v_add_f32_dpp v224, v224, v224 row_mirror row_mask:0xf bank_mask:0xf bound_ctrl:1
	v_add_f32_e32 v86, 1.0, v86
	v_exp_f32_e32 v27, v27
	v_mov_b32_dpp v226, v224 row_bcast:15 row_mask:0xa bank_mask:0xf
	v_add_f32_e32 v224, v224, v226
	v_mov_b32_e32 v226, 0
	v_mul_f32_e32 v229, v233, v27
	v_sub_f32_e32 v219, v219, v97
	v_mov_b32_dpp v226, v224 row_bcast:31 row_mask:0xc bank_mask:0xf
	v_add_f32_e32 v224, v224, v226
	v_fma_f32 v219, v40, v219, v97
	v_readlane_b32 s0, v224, 63
	v_add_f32_e32 v27, v95, v92
	v_add_f32_e32 v92, v94, v93
	v_max_f32_e64 v224, s0, s0
	v_max_f32_e32 v224, 0x179abe15, v224
	v_rsq_f32_e32 v226, v224
	v_rcp_f32_e32 v224, v86
	v_mul_f32_e32 v86, 0xbfb8aa3b, v87
	v_exp_f32_e32 v232, v86
	v_mul_f32_e32 v226, v218, v226
	v_add_f32_e32 v86, -1.0, v224
	v_fma_f32 v227, v3, v86, 1.0
	v_rcp_f32_e32 v86, v229
	v_sub_f32_e32 v97, v97, v213
	v_sub_f32_e32 v96, v96, v212
	v_xor_b32_e32 v218, 0x80000000, v226
	v_pk_mul_f32 v[86:87], v[222:223], v[86:87] op_sel_hi:[1,0]
	v_pk_mul_f32 v[222:223], v[224:225], v[226:227]
	v_fma_f32 v225, v40, v97, v213
	v_fma_f32 v227, v42, v96, v212
	v_pk_add_f32 v[96:97], v[36:37], v[34:35] neg_lo:[0,1] neg_hi:[0,1]
	v_mul_f32_e32 v37, 0xbfb8aa3b, v92
	v_exp_f32_e32 v37, v37
	v_mul_f32_e64 v93, |v27|, s79
	v_exp_f32_e32 v93, v93
	v_sub_f32_e32 v213, v213, v43
	v_add_f32_e32 v37, 1.0, v37
	v_rcp_f32_e32 v226, v37
	v_add_f32_e32 v93, 1.0, v93
	v_log_f32_e32 v93, v93
	v_fmac_f32_e32 v43, v40, v213
	v_add_f32_e32 v37, -1.0, v226
	v_fma_f32 v231, v3, v37, 1.0
	v_add_f32_e32 v37, v95, v217
	v_mul_f32_e64 v95, |v37|, s79
; __device__ __forceinline__ unsigned cvt_pk_bf16_nat(float lo, float hi) { const f32x2n v = {lo, hi}; return __builtin_bit_cast(unsigned, __builtin_convertvector(v, bf16x2n)); }
; __device__ __forceinline__ float fast_sigmoid(float x) { return __builtin_amdgcn_rcpf(1.0f + __builtin_amdgcn_exp2f(-1.4426950408889634f * x)); }
; __global__ void __launch_bounds__(NTHR, 2) mk_fwd(Args args) {
;     ...
;                     for (int t = 0; t < 16; ++t) {
;                         const float cr = xr_[t + 1], ck = xk_[t + 1], cv = xv_[t + 1], wl = xwl_[t] + c_w0, al = xal_[t] + c_a0;
;                         const float pr_r = xr_[t], pr_k = xk_[t], pr_v = xv_[t];
;                         const float r = cr + (pr_r - cr) * mu_r, k = ck + (pr_k - ck) * mu_k, v = cv + (pr_v - cv) * mu_v;
;                         const float dec = fast_decay(wl), a = fast_sigmoid(al);
;                         float kk = k * c_kk; const float ss = wave_sum_dpp(kk * kk); kk = kk * __builtin_amdgcn_rsqf(fmaxf(ss, 1e-24f));
;                         const float k2 = k * (1.0f + (a - 1.0f) * c_ka), bb = kk * a;
;                         const float Wprev = Wc; Wc = Wc * dec; const float iw = __builtin_amdgcn_rcpf(Wc);
;                         At[t] = -kk * Wprev; Rt[t] = r * Wc; Bt[t] = bb * iw; Kt[t] = k2 * iw; Vt[t] = v;
;                     }
; #pragma unroll
;                     for (int t = 0; t < 16; ++t) {
;                         const unsigned ar_ = cvt_pk_bf16_nat(At[t], Rt[t]), bk_ = cvt_pk_bf16_nat(Bt[t], Kt[t]); const bf16 ab = (bf16)ar_, rb = (bf16)(ar_ >> 16);
;                         IMG[0 * 1152 + t * 72 + pos] = ab; IMG[1 * 1152 + t * 72 + pos] = rb; IMG[2 * 1152 + t * 72 + pos] = (bf16)bk_; IMG[3 * 1152 + t * 72 + pos] = (bf16)(bk_ >> 16);
;                     }
	v_exp_f32_e32 v95, v95
	v_max_f32_e64 v27, -v27, 0
	v_mul_f32_e32 v92, v28, v227
	v_fmac_f32_e32 v27, 0x3f317218, v93
	v_add_f32_e32 v40, 1.0, v95
	v_sub_f32_e32 v95, v212, v41
	v_fmac_f32_e32 v41, v42, v95
	v_mul_f32_e32 v93, v92, v92
	v_mul_f32_e32 v28, v28, v41
	v_mul_f32_e32 v42, v28, v28
	v_mov_b32_dpp v93, v93 quad_perm:[1,0,3,2] row_mask:0xf bank_mask:0xf bound_ctrl:1
	v_fmac_f32_e32 v93, v92, v92
	v_log_f32_e32 v40, v40
	v_mov_b32_dpp v42, v42 quad_perm:[1,0,3,2] row_mask:0xf bank_mask:0xf bound_ctrl:1
	v_add_f32_dpp v93, v93, v93 quad_perm:[2,3,0,1] row_mask:0xf bank_mask:0xf bound_ctrl:1
	v_fmac_f32_e32 v42, v28, v28
	v_mov_b32_e32 v224, 0
	v_add_f32_dpp v93, v93, v93 row_half_mirror row_mask:0xf bank_mask:0xf bound_ctrl:1
	v_add_f32_dpp v42, v42, v42 quad_perm:[2,3,0,1] row_mask:0xf bank_mask:0xf bound_ctrl:1
	v_add_f32_e32 v94, v94, v216
	v_add_f32_dpp v93, v93, v93 row_mirror row_mask:0xf bank_mask:0xf bound_ctrl:1
	v_max_f32_e64 v37, -v37, 0
	v_add_f32_dpp v42, v42, v42 row_half_mirror row_mask:0xf bank_mask:0xf bound_ctrl:1
	v_mov_b32_dpp v224, v93 row_bcast:15 row_mask:0xa bank_mask:0xf
	v_fmac_f32_e32 v37, 0x3f317218, v40
	v_mul_f32_e32 v40, 0xbfb8aa3b, v94
	v_add_f32_dpp v42, v42, v42 row_mirror row_mask:0xf bank_mask:0xf bound_ctrl:1
	v_mov_b32_e32 v94, 0
	v_add_f32_e32 v93, v93, v224
	v_mov_b32_e32 v224, 0
	v_mov_b32_dpp v94, v42 row_bcast:15 row_mask:0xa bank_mask:0xf
	v_add_f32_e32 v42, v42, v94
	v_mov_b32_dpp v224, v93 row_bcast:31 row_mask:0xc bank_mask:0xf
	v_mov_b32_e32 v94, 0
	v_add_f32_e32 v27, 0.5, v27
	v_add_f32_e32 v93, v93, v224
	v_exp_f32_e32 v40, v40
	v_mov_b32_dpp v94, v42 row_bcast:31 row_mask:0xc bank_mask:0xf
	v_mul_f32_e32 v27, 0xbfb8aa3b, v27
	v_readlane_b32 s0, v93, 63
	v_add_f32_e32 v42, v42, v94
	v_exp_f32_e32 v27, v27
	v_max_f32_e64 v93, s0, s0
	v_readlane_b32 s0, v42, 63
	v_add_f32_e32 v40, 1.0, v40
	v_rcp_f32_e32 v40, v40
	v_max_f32_e64 v42, s0, s0
	v_max_f32_e32 v42, 0x179abe15, v42
	v_rsq_f32_e32 v42, v42
	v_mul_f32_e32 v27, 0xbfb8aa3b, v27
	v_exp_f32_e32 v27, v27
	v_xor_b32_e32 v220, 0x80000000, v228
	v_mul_f32_e32 v212, v28, v42
	v_add_f32_e32 v28, -1.0, v40
	v_mov_b32_e32 v228, v233
	v_mul_f32_e32 v233, v229, v232
	v_fma_f32 v213, v3, v28, 1.0
	v_cvt_pk_bf16_f32 v3, v214, v215
	v_add_f32_e32 v37, 0.5, v37
	v_mul_f32_e32 v217, v233, v27
	v_cvt_pk_bf16_f32 v27, v38, v39
	ds_write_b16 v101, v3
	ds_write_b16_d16_hi v101, v3 offset:2304
	ds_write_b16 v101, v27 offset:4608
	ds_write_b16_d16_hi v101, v27 offset:6912
	v_cvt_pk_bf16_f32 v3, v50, v51
	v_mul_f32_e32 v37, 0xbfb8aa3b, v37
	v_cvt_pk_bf16_f32 v27, v44, v45
	ds_write_b16 v101, v3 offset:144
	ds_write_b16_d16_hi v101, v3 offset:2448
	ds_write_b16 v101, v27 offset:4752
	ds_write_b16_d16_hi v101, v27 offset:7056
	v_cvt_pk_bf16_f32 v3, v54, v55
	v_max_f32_e32 v93, 0x179abe15, v93
	v_exp_f32_e32 v37, v37
	v_cvt_pk_bf16_f32 v27, v46, v47
	ds_write_b16 v101, v3 offset:288
	ds_write_b16_d16_hi v101, v3 offset:2592
	ds_write_b16 v101, v27 offset:4896
	ds_write_b16_d16_hi v101, v27 offset:7200
	v_cvt_pk_bf16_f32 v3, v60, v61
	v_rsq_f32_e32 v93, v93
	v_cvt_pk_bf16_f32 v27, v48, v49
	ds_write_b16 v101, v3 offset:432
	ds_write_b16_d16_hi v101, v3 offset:2736
	ds_write_b16 v101, v27 offset:5040
	ds_write_b16_d16_hi v101, v27 offset:7344
	v_cvt_pk_bf16_f32 v3, v64, v65
	v_cvt_pk_bf16_f32 v27, v52, v53
	ds_write_b16 v101, v3 offset:576
	ds_write_b16_d16_hi v101, v3 offset:2880
	ds_write_b16 v101, v27 offset:5184
	ds_write_b16_d16_hi v101, v27 offset:7488
	v_cvt_pk_bf16_f32 v3, v68, v69
	v_cvt_pk_bf16_f32 v27, v56, v57
	ds_write_b16 v101, v3 offset:720
	ds_write_b16_d16_hi v101, v3 offset:3024
	ds_write_b16 v101, v27 offset:5328
	ds_write_b16_d16_hi v101, v27 offset:7632
	v_cvt_pk_bf16_f32 v3, v72, v73
	v_mul_f32_e32 v37, 0xbfb8aa3b, v37
	v_cvt_pk_bf16_f32 v27, v62, v63
	ds_write_b16 v101, v3 offset:864
	ds_write_b16_d16_hi v101, v3 offset:3168
	ds_write_b16 v101, v27 offset:5472
	ds_write_b16_d16_hi v101, v27 offset:7776
	v_cvt_pk_bf16_f32 v3, v76, v77
	v_mul_f32_e32 v230, v92, v93
	v_rcp_f32_e32 v92, v233
	v_exp_f32_e32 v37, v37
; __device__ __forceinline__ unsigned cvt_pk_bf16_nat(float lo, float hi) { const f32x2n v = {lo, hi}; return __builtin_bit_cast(unsigned, __builtin_convertvector(v, bf16x2n)); }
; __device__ __forceinline__ unsigned pk2(float lo, float hi) { return cvt_pk_bf16_nat(lo, hi); }
; __device__ __forceinline__ float fast_sigmoid(float x) { return __builtin_amdgcn_rcpf(1.0f + __builtin_amdgcn_exp2f(-1.4426950408889634f * x)); }
; __global__ void __launch_bounds__(NTHR, 2) mk_fwd(Args args) {
;     ...
;                         const float cr = xr_[t + 1], ck = xk_[t + 1], cv = xv_[t + 1], wl = xwl_[t] + c_w0, al = xal_[t] + c_a0;
;                         const float pr_r = xr_[t], pr_k = xk_[t], pr_v = xv_[t];
;                         const float r = cr + (pr_r - cr) * mu_r, k = ck + (pr_k - ck) * mu_k, v = cv + (pr_v - cv) * mu_v;
;                         const float dec = fast_decay(wl), a = fast_sigmoid(al);
;                         float kk = k * c_kk; const float ss = wave_sum_dpp(kk * kk); kk = kk * __builtin_amdgcn_rsqf(fmaxf(ss, 1e-24f));
;                         const float k2 = k * (1.0f + (a - 1.0f) * c_ka), bb = kk * a;
;                         const float Wprev = Wc; Wc = Wc * dec; const float iw = __builtin_amdgcn_rcpf(Wc);
;                         At[t] = -kk * Wprev; Rt[t] = r * Wc; Bt[t] = bb * iw; Kt[t] = k2 * iw; Vt[t] = v;
;                     }
; #pragma unroll
;                     for (int t = 0; t < 16; ++t) {
;                         const unsigned ar_ = cvt_pk_bf16_nat(At[t], Rt[t]), bk_ = cvt_pk_bf16_nat(Bt[t], Kt[t]); const bf16 ab = (bf16)ar_, rb = (bf16)(ar_ >> 16);
;                         IMG[0 * 1152 + t * 72 + pos] = ab; IMG[1 * 1152 + t * 72 + pos] = rb; IMG[2 * 1152 + t * 72 + pos] = (bf16)bk_; IMG[3 * 1152 + t * 72 + pos] = (bf16)(bk_ >> 16);
;                     }
; #pragma unroll
;                     for (int qq = 0; qq < 4; ++qq) { v4u o; o.x = pk2(Bt[4 * qq] * Wc, Bt[4 * qq + 1] * Wc); o.y = pk2(Bt[4 * qq + 2] * Wc, Bt[4 * qq + 3] * Wc); o.z = pk2(Kt[4 * qq] * Wc, Kt[4 * qq + 1] * Wc); o.w = pk2(Kt[4 * qq + 2] * Wc, Kt[4 * qq + 3] * Wc);
	v_cvt_pk_bf16_f32 v27, v66, v67
	ds_write_b16 v101, v3 offset:1008
	ds_write_b16_d16_hi v101, v3 offset:3312
	ds_write_b16 v101, v27 offset:5616
	ds_write_b16_d16_hi v101, v27 offset:7920
	v_cvt_pk_bf16_f32 v3, v80, v81
	v_rcp_f32_e32 v28, v217
	v_cvt_pk_bf16_f32 v27, v70, v71
	ds_write_b16 v101, v3 offset:1152
	ds_write_b16_d16_hi v101, v3 offset:3456
	ds_write_b16 v101, v27 offset:5760
	ds_write_b16_d16_hi v101, v27 offset:8064
	v_cvt_pk_bf16_f32 v3, v82, v83
	v_cvt_pk_bf16_f32 v27, v74, v75
	ds_write_b16 v101, v3 offset:1296
	ds_write_b16_d16_hi v101, v3 offset:3600
	ds_write_b16 v101, v27 offset:5904
	ds_write_b16_d16_hi v101, v27 offset:8208
	v_cvt_pk_bf16_f32 v3, v88, v89
	v_pk_mul_f32 v[220:221], v[228:229], v[220:221]
	v_mov_b32_e32 v232, v229
	v_cvt_pk_bf16_f32 v27, v78, v79
	ds_write_b16 v101, v3 offset:1440
	ds_write_b16_d16_hi v101, v3 offset:3744
	ds_write_b16 v101, v27 offset:6048
	ds_write_b16_d16_hi v101, v27 offset:8352
	v_cvt_pk_bf16_f32 v3, v90, v91
	v_xor_b32_e32 v224, 0x80000000, v230
	v_pk_mul_f32 v[218:219], v[232:233], v[218:219]
	v_pk_mul_f32 v[92:93], v[222:223], v[92:93] op_sel_hi:[1,0]
	v_pk_mul_f32 v[222:223], v[226:227], v[230:231]
	v_mov_b32_e32 v216, v233
	v_mul_f32_e32 v95, v217, v37
	v_cvt_pk_bf16_f32 v27, v84, v85
	ds_write_b16 v101, v3 offset:1584
	ds_write_b16_d16_hi v101, v3 offset:3888
	ds_write_b16 v101, v27 offset:6192
	ds_write_b16_d16_hi v101, v27 offset:8496
	v_cvt_pk_bf16_f32 v3, v220, v221
	v_xor_b32_e32 v42, 0x80000000, v212
	v_pk_mul_f32 v[224:225], v[216:217], v[224:225]
	v_pk_mul_f32 v[222:223], v[222:223], v[28:29] op_sel_hi:[1,0]
	v_rcp_f32_e32 v28, v95
	v_mov_b32_e32 v94, v217
	v_cvt_pk_bf16_f32 v27, v86, v87
	ds_write_b16 v101, v3 offset:1728
	ds_write_b16_d16_hi v101, v3 offset:4032
	ds_write_b16 v101, v27 offset:6336
	ds_write_b16_d16_hi v101, v27 offset:8640
	v_cvt_pk_bf16_f32 v3, v218, v219
	v_pk_mul_f32 v[42:43], v[94:95], v[42:43]
	v_cvt_pk_bf16_f32 v27, v92, v93
	ds_write_b16 v101, v3 offset:1872
	ds_write_b16_d16_hi v101, v3 offset:4176
	ds_write_b16 v101, v27 offset:6480
	ds_write_b16_d16_hi v101, v27 offset:8784
	v_cvt_pk_bf16_f32 v3, v224, v225
	v_cvt_pk_bf16_f32 v27, v222, v223
	ds_write_b16 v101, v3 offset:2016
	ds_write_b16_d16_hi v101, v3 offset:4320
	ds_write_b16 v101, v27 offset:6624
	ds_write_b16_d16_hi v101, v27 offset:8928
	v_cvt_pk_bf16_f32 v3, v42, v43
	v_mov_b32_e32 v42, v5
	v_mov_b32_e32 v43, v20
	v_pk_mul_f32 v[40:41], v[40:41], v[212:213]
	v_pk_add_f32 v[4:5], v[4:5], v[42:43] neg_lo:[0,1] neg_hi:[0,1]
	v_pk_mul_f32 v[40:41], v[40:41], v[28:29] op_sel_hi:[1,0]
	v_pk_fma_f32 v[42:43], v[2:3], v[4:5], v[42:43] op_sel_hi:[0,1,1]
	v_pk_mov_b32 v[4:5], v[20:21], v[22:23] op_sel:[1,0]
	v_cvt_pk_bf16_f32 v27, v40, v41
	v_pk_add_f32 v[20:21], v[20:21], v[4:5] neg_lo:[0,1] neg_hi:[0,1]
	v_mov_b32_e32 v28, v25
	v_pk_fma_f32 v[20:21], v[2:3], v[20:21], v[4:5] op_sel_hi:[0,1,1]
	v_pk_mov_b32 v[4:5], v[22:23], v[26:27] op_sel:[1,0]
	ds_write_b16 v101, v3 offset:2160
	ds_write_b16_d16_hi v101, v3 offset:4464
	ds_write_b16 v101, v27 offset:6768
	ds_write_b16_d16_hi v101, v27 offset:9072
	v_pk_add_f32 v[22:23], v[22:23], v[4:5] neg_lo:[0,1] neg_hi:[0,1]
	v_pk_fma_f32 v[26:27], v[2:3], v[58:59], v[24:25] op_sel_hi:[0,1,1]
	v_pk_fma_f32 v[22:23], v[2:3], v[22:23], v[4:5] op_sel_hi:[0,1,1]
	v_mov_b32_e32 v4, v29
	v_mov_b32_e32 v5, v30
	v_pk_add_f32 v[24:25], v[28:29], v[4:5] neg_lo:[0,1] neg_hi:[0,1]
	v_mov_b32_e32 v50, v95
	v_pk_fma_f32 v[24:25], v[2:3], v[24:25], v[4:5] op_sel_hi:[0,1,1]
	v_pk_mov_b32 v[4:5], v[30:31], v[32:33] op_sel:[1,0]
	s_mov_b64 s[0:1], 0x1c00
	v_pk_add_f32 v[28:29], v[30:31], v[4:5] neg_lo:[0,1] neg_hi:[0,1]
	s_mov_b32 s34, 0
	v_pk_fma_f32 v[28:29], v[2:3], v[28:29], v[4:5] op_sel_hi:[0,1,1]
	v_pk_mov_b32 v[4:5], v[32:33], v[36:37] op_sel:[1,0]
	s_nop 0
	v_pk_add_f32 v[30:31], v[32:33], v[4:5] neg_lo:[0,1] neg_hi:[0,1]
	v_pk_fma_f32 v[32:33], v[2:3], v[96:97], v[34:35] op_sel_hi:[0,1,1]
	v_pk_fma_f32 v[30:31], v[2:3], v[30:31], v[4:5] op_sel_hi:[0,1,1]
	v_mov_b32_e32 v2, v38
	v_mov_b32_e32 v3, v44
	v_mov_b32_e32 v4, v46
	v_mov_b32_e32 v5, v48
